# NA attention: waves skip QK/PV MFMAs and exps for tiles fully outside their window (exact zeros), flags in s100/s101
# speedup vs baseline: 1.0149x; 1.0013x over previous
.LBB0_528:
	s_mov_b32 s100, 0
	s_mov_b32 s101, 0
	s_or_b64 exec, exec, s[4:5]
	v_mbcnt_lo_u32_b32 v18, -1, 0
	v_mbcnt_hi_u32_b32 v18, -1, v18
	v_cmp_gt_u32_e32 vcc, 16, v18
	v_lshlrev_b32_e32 v19, 2, v18
	v_add_u32_e32 v19, 0x16000, v19
	v_cndmask_b32_e64 v20, v242, 0, vcc
	ds_write_b32 v19, v242
	ds_write_b32 v19, v20 offset:256
	s_and_b32 s4, s0, 0x3fffffc0
	s_ashr_i32 s65, s0, 7
	s_lshl_b32 s0, s4, 2
	s_add_i32 s6, s0, 0
	s_max_i32 s0, s63, 1
	s_add_i32 s0, s0, -1
	s_min_u32 s12, s0, 56
	s_add_i32 s12, s12, 7
	s_sub_i32 s7, s12, s1
	s_add_i32 s0, s7, 5
	s_and_b32 s13, s0, 1
	s_max_i32 s46, s57, 4
	s_add_i32 s0, s13, s0
	s_cmp_lg_u32 0, -1
	s_cselect_b32 s4, 0, 0
	v_lshlrev_b32_e32 v0, 10, v216
	v_lshlrev_b32_e32 v18, 4, v213
	s_add_i32 s4, s4, s23
	v_add3_u32 v227, 0, v0, v18
	v_lshl_add_u64 v[18:19], v[36:37], 0, s[20:21]
	s_add_i32 s5, s4, 0x4000
	s_mov_b32 s23, m0
	s_mov_b32 m0, s5
	s_nop 0
	global_load_lds_dwordx4 v[18:19], off
	s_mov_b32 m0, s23
	s_waitcnt vmcnt(3) lgkmcnt(0)
	s_barrier
	ds_read_b128 v[40:43], v227
	ds_read_b128 v[44:47], v227 offset:512
	s_waitcnt vmcnt(1) lgkmcnt(1)
	v_mfma_f32_32x32x16_bf16 v[18:33], v[40:43], v[156:159], v[2:17]
	v_and_or_b32 v39, s59, 32, v213
	v_sub_u32_e32 v224, 15, v39
	s_mov_b64 s[26:27], 0x288000
	s_add_i32 s4, s4, 0x8000
	v_lshlrev_b32_e32 v0, 1, v38
	v_and_b32_e32 v219, 32, v0
	v_lshlrev_b32_e32 v0, 2, v216
	s_waitcnt lgkmcnt(0)
	v_mfma_f32_32x32x16_bf16 v[2:17], v[44:47], v[156:159], v[2:17]
	ds_read_b128 v[40:43], v227 offset:2048
	ds_read_b128 v[44:47], v227 offset:2560
	v_lshrrev_b32_e32 v38, 2, v38
	v_and_or_b32 v38, v38, 3, v0
	v_lshlrev_b32_e32 v218, 6, v38
	v_add_u32_e32 v38, 0, v219
	v_add3_u32 v226, v38, v217, v218
	v_lshl_add_u32 v225, v216, 4, s77
	s_waitcnt lgkmcnt(1)
	v_mfma_f32_32x32x16_bf16 v[18:33], v[40:43], v[152:155], v[18:33]
	s_mov_b32 s23, 1
	s_mov_b32 s47, 0
	s_movk_i32 s81, 0x4000
	s_cmp_gt_i32 s0, 6
	v_lshl_add_u32 v228, v224, 2, v225
	v_lshl_add_u64 v[196:197], v[34:35], 0, s[2:3]
	v_lshl_add_u32 v221, v213, 2, s6
	s_waitcnt lgkmcnt(0)
	v_mfma_f32_32x32x16_bf16 v[2:17], v[44:47], v[152:155], v[2:17]
	ds_read_b128 v[40:43], v227 offset:4096
	ds_read_b128 v[44:47], v227 offset:4608
	v_lshl_add_u32 v220, v0, 2, s6
	s_waitcnt lgkmcnt(1)
	v_mfma_f32_32x32x16_bf16 v[18:33], v[40:43], v[148:151], v[18:33]
	ds_read_b128 v[40:43], v227 offset:6656
	ds_read_b128 v[48:51], v227 offset:6144
	s_waitcnt lgkmcnt(2)
	v_mfma_f32_32x32x16_bf16 v[2:17], v[44:47], v[148:151], v[2:17]
	v_sub_u32_e64 v44, v39, 8 clamp
	v_min_u32_e32 v38, 48, v44
	v_sub_u32_e32 v223, v0, v38
	s_waitcnt vmcnt(0) lgkmcnt(0)
	v_mfma_f32_32x32x16_bf16 v[18:33], v[48:51], v[144:147], v[18:33]
	v_mfma_f32_32x32x16_bf16 v[2:17], v[40:43], v[144:147], v[2:17]
	s_nop 15
	s_nop 7
	s_nop 0
	v_max3_f32 v39, v18, v19, v2
	v_max3_f32 v40, v20, v21, v3
	s_nop 0
	v_max3_f32 v39, v39, v4, v5
	v_max3_f32 v40, v40, v24, v25
	s_nop 0
	v_max3_f32 v39, v39, v22, v23
	v_max3_f32 v40, v40, v8, v9
	s_nop 0
	v_max3_f32 v39, v39, v6, v7
	v_max3_f32 v40, v40, v28, v29
	s_nop 0
	v_max3_f32 v39, v39, v26, v27
	v_max3_f32 v40, v40, v12, v13
	s_nop 0
	v_max3_f32 v39, v39, v10, v11
	v_max3_f32 v40, v40, v32, v33
	s_nop 0
	v_max3_f32 v39, v39, v30, v31
	v_max3_f32 v40, v40, v16, v17
	s_nop 0
	v_max3_f32 v39, v39, v14, v15
	s_nop 0
	v_max_f32_e32 v39, v39, v40
	s_nop 0
	v_mov_b32_e32 v40, v39
	s_nop 1
	v_permlane32_swap_b32_e32 v39, v40
	v_max_f32_e32 v39, v39, v40
	s_nop 0
	v_add_f32_e32 v222, v1, v39
	v_sub_f32_e32 v2, v2, v39
	v_sub_f32_e32 v3, v3, v39
	v_sub_f32_e32 v18, v18, v39
	v_sub_f32_e32 v19, v19, v39
	v_sub_f32_e32 v20, v20, v39
	s_nop 0
	v_xor_b32_e32 v48, 0x80000000, v222
	v_mov_b32_e32 v49, v48
	v_mov_b32_e32 v50, v48
	v_mov_b32_e32 v51, v48
	v_mov_b32_e32 v52, v48
	v_mov_b32_e32 v53, v48
	v_mov_b32_e32 v54, v48
	v_mov_b32_e32 v55, v48
	v_mov_b32_e32 v56, v48
	v_mov_b32_e32 v57, v48
	v_mov_b32_e32 v58, v48
	v_mov_b32_e32 v59, v48
	v_mov_b32_e32 v60, v48
	v_mov_b32_e32 v61, v48
	v_mov_b32_e32 v62, v48
	v_mov_b32_e32 v63, v48
	s_waitcnt vmcnt(0) lgkmcnt(0)
	s_barrier
	v_exp_f32_e32 v64, v2
	v_exp_f32_e32 v65, v3
	v_lshl_add_u64 v[2:3], v[36:37], 0, s[26:27]
	s_mov_b32 s5, m0
	s_mov_b32 m0, s8
	s_nop 0
	global_load_lds_dwordx4 v[2:3], off
	s_mov_b32 m0, s5
	v_lshl_add_u64 v[2:3], v[204:205], 0, s[70:71]
	s_mov_b32 s5, m0
	s_mov_b32 m0, s4
	s_nop 0
	global_load_lds_dwordx4 v[2:3], off
	s_mov_b32 m0, s5
	ds_read_b128 v[188:191], v227 offset:8192
	ds_read_b128 v[184:187], v227 offset:8704
	ds_read_b128 v[180:183], v227 offset:10240
	ds_read_b128 v[176:179], v227 offset:10752
	ds_read_b128 v[172:175], v227 offset:12288
	ds_read_b128 v[168:171], v227 offset:12800
	ds_read_b128 v[164:167], v227 offset:14336
	ds_read_b128 v[160:163], v227 offset:14848
	v_sub_f32_e32 v4, v4, v39
	v_sub_f32_e32 v21, v21, v39
	v_sub_f32_e32 v5, v5, v39
	v_sub_f32_e32 v22, v22, v39
	v_sub_f32_e32 v6, v6, v39
	v_sub_f32_e32 v23, v23, v39
	v_sub_f32_e32 v7, v7, v39
	v_sub_f32_e32 v24, v24, v39
	v_sub_f32_e32 v8, v8, v39
	v_sub_f32_e32 v25, v25, v39
	v_sub_f32_e32 v9, v9, v39
	v_sub_f32_e32 v26, v26, v39
	v_sub_f32_e32 v10, v10, v39
	v_sub_f32_e32 v27, v27, v39
	v_sub_f32_e32 v11, v11, v39
	v_sub_f32_e32 v28, v28, v39
	v_sub_f32_e32 v12, v12, v39
	v_sub_f32_e32 v29, v29, v39
	v_sub_f32_e32 v13, v13, v39
	v_sub_f32_e32 v30, v30, v39
	v_sub_f32_e32 v14, v14, v39
	v_sub_f32_e32 v31, v31, v39
	v_sub_f32_e32 v15, v15, v39
	v_sub_f32_e32 v32, v32, v39
	v_sub_f32_e32 v16, v16, v39
	v_sub_f32_e32 v33, v33, v39
	v_sub_f32_e32 v17, v17, v39
	v_exp_f32_e32 v80, v18
	v_exp_f32_e32 v81, v19
	v_exp_f32_e32 v82, v20
	v_exp_f32_e32 v83, v21
	v_exp_f32_e32 v84, v22
	v_exp_f32_e32 v85, v23
	v_exp_f32_e32 v86, v24
	v_exp_f32_e32 v87, v25
	v_exp_f32_e32 v88, v26
	v_exp_f32_e32 v89, v27
	v_exp_f32_e32 v90, v28
	v_exp_f32_e32 v91, v29
	v_exp_f32_e32 v92, v30
	v_exp_f32_e32 v93, v31
	v_exp_f32_e32 v94, v32
	v_exp_f32_e32 v95, v33
	v_exp_f32_e32 v66, v4
	v_exp_f32_e32 v67, v5
	v_exp_f32_e32 v68, v6
	v_exp_f32_e32 v69, v7
	v_exp_f32_e32 v70, v8
	v_exp_f32_e32 v71, v9
	v_exp_f32_e32 v72, v10
	v_exp_f32_e32 v73, v11
	v_exp_f32_e32 v74, v12
	v_exp_f32_e32 v75, v13
	v_exp_f32_e32 v76, v14
	v_exp_f32_e32 v77, v15
	v_exp_f32_e32 v78, v16
	v_exp_f32_e32 v79, v17
	s_waitcnt vmcnt(2) lgkmcnt(0)
	s_barrier
	v_cmp_gt_u32_e64 s[4:5], 32, v211
	s_cbranch_scc0 .LBB0_618
	s_mul_i32 s6, s46, 0xd8000
	s_add_i32 s68, s6, 0xffca0000
	s_add_i32 s6, s46, s56
	s_sub_i32 s49, s6, s65
	s_add_i32 s6, s65, s57
	s_max_i32 s6, s6, 4
	s_add_i32 s6, s6, -4
	v_mov_b32_e32 v14, v1
	v_mov_b32_e32 v15, v1
	s_min_u32 s6, s6, 56
	v_mov_b32_e32 v0, v1
	v_mov_b32_e32 v2, v1
	v_mov_b32_e32 v3, v1
	v_mov_b32_e32 v4, v1
	v_mov_b32_e32 v5, v1
	v_mov_b32_e32 v6, v1
	v_mov_b32_e32 v7, v1
	v_mov_b32_e32 v8, v1
	v_mov_b32_e32 v9, v1
	v_mov_b32_e32 v10, v1
	v_mov_b32_e32 v11, v1
	v_mov_b32_e32 v12, v1
	v_mov_b32_e32 v13, v1
	v_mov_b64_e32 v[46:47], v[14:15]
	v_mov_b64_e32 v[30:31], v[14:15]
	s_add_i32 s48, s13, s7
	s_sub_i32 s50, s46, s6
	v_lshl_add_u64 v[198:199], v[196:197], 0, s[68:69]
	s_mov_b32 s44, 0
	s_movk_i32 s47, 0x4000
	s_movk_i32 s64, 0x2000
	v_mov_b32_e32 v229, 0
	s_mov_b32 s23, -2
	s_mov_b64 s[6:7], s[72:73]
	v_mov_b64_e32 v[44:45], v[12:13]
	v_mov_b64_e32 v[42:43], v[10:11]
	v_mov_b64_e32 v[40:41], v[8:9]
	v_mov_b64_e32 v[38:39], v[6:7]
	v_mov_b64_e32 v[36:37], v[4:5]
	v_mov_b64_e32 v[34:35], v[2:3]
	v_mov_b64_e32 v[32:33], v[0:1]
	v_mov_b64_e32 v[28:29], v[12:13]
	v_mov_b64_e32 v[26:27], v[10:11]
	v_mov_b64_e32 v[24:25], v[8:9]
	v_mov_b64_e32 v[22:23], v[6:7]
	v_mov_b64_e32 v[20:21], v[4:5]
	v_mov_b64_e32 v[18:19], v[2:3]
	v_mov_b64_e32 v[16:17], v[0:1]
.LBB0_530:
	v_add_co_u32_e64 v0, s[42:43], s23, 3
	s_nop 0
	v_readfirstlane_b32 s26, v0
	s_add_i32 s27, s64, s8
	s_mov_b32 s101, s100
	s_mov_b32 s100, 0
	s_cmp_lt_u32 s26, 4
	s_cbranch_scc1 .Lna_ent_0
	s_add_i32 vcc_lo, s50, s23
	s_add_i32 vcc_lo, vcc_lo, -5
	s_cmp_gt_u32 vcc_lo, 7
	s_cselect_b32 s100, 1, 0
	s_cbranch_scc1 .Lna_skA_0
.Lna_ent_0:
	v_add_u32_e32 v0, s44, v226
	ds_read_b64_tr_b16 v[192:193], v0 offset:24576
	ds_read_b64_tr_b16 v[194:195], v0 offset:25088
	s_waitcnt lgkmcnt(9)
	v_mfma_f32_32x32x16_bf16 v[112:127], v[188:191], v[156:159], v[48:63]
	v_add_f32_e32 v2, v80, v81
	v_add_f32_e32 v2, v82, v2
	v_add_f32_e32 v2, v83, v2
	v_add_f32_e32 v2, v84, v2
	v_add_f32_e32 v2, v85, v2
	v_cvt_pk_bf16_f32 v140, v80, v81
	v_cvt_pk_bf16_f32 v141, v82, v83
	ds_read_b64_tr_b16 v[10:11], v0 offset:28672
	ds_read_b64_tr_b16 v[12:13], v0 offset:29184
	s_waitcnt lgkmcnt(10)
	v_mfma_f32_32x32x16_bf16 v[96:111], v[184:187], v[156:159], v[48:63]
	v_add_f32_e32 v2, v86, v2
	v_add_f32_e32 v2, v87, v2
	v_add_f32_e32 v2, v88, v2
	v_add_f32_e32 v6, v89, v2
	v_cvt_pk_bf16_f32 v142, v84, v85
	v_cvt_pk_bf16_f32 v143, v86, v87
	ds_read_b64_tr_b16 v[2:3], v0 offset:25600
	ds_read_b64_tr_b16 v[4:5], v0 offset:26112
	s_waitcnt lgkmcnt(11)
	v_mfma_f32_32x32x16_bf16 v[112:127], v[180:183], v[152:155], v[112:127]
	v_add_f32_e32 v6, v90, v6
	v_add_f32_e32 v6, v91, v6
	v_add_f32_e32 v6, v92, v6
	v_add_f32_e32 v14, v93, v6
	v_cvt_pk_bf16_f32 v136, v88, v89
	v_cvt_pk_bf16_f32 v137, v90, v91
	ds_read_b64_tr_b16 v[6:7], v0 offset:29696
	ds_read_b64_tr_b16 v[8:9], v0 offset:30208
	s_waitcnt lgkmcnt(12)
	v_mfma_f32_32x32x16_bf16 v[96:111], v[176:179], v[152:155], v[96:111]
	v_add_f32_e32 v14, v94, v14
	v_add_f32_e32 v14, v95, v14
	v_add_f32_e32 v14, v64, v14
	v_add_f32_e32 v14, v65, v14
	v_cvt_pk_bf16_f32 v138, v92, v93
	v_cvt_pk_bf16_f32 v139, v94, v95
	ds_read_b64_tr_b16 v[80:81], v0 offset:26624
	ds_read_b64_tr_b16 v[82:83], v0 offset:27136
	s_waitcnt lgkmcnt(13)
	v_mfma_f32_32x32x16_bf16 v[112:127], v[172:175], v[148:151], v[112:127]
	v_add_f32_e32 v14, v66, v14
	v_add_f32_e32 v14, v67, v14
	v_add_f32_e32 v14, v68, v14
	v_add_f32_e32 v14, v69, v14
	v_cvt_pk_bf16_f32 v132, v64, v65
	v_cvt_pk_bf16_f32 v133, v66, v67
	ds_read_b64_tr_b16 v[84:85], v0 offset:30720
	ds_read_b64_tr_b16 v[86:87], v0 offset:31232
	s_waitcnt lgkmcnt(14)
	v_mfma_f32_32x32x16_bf16 v[96:111], v[168:171], v[148:151], v[96:111]
	v_add_f32_e32 v14, v70, v14
	v_add_f32_e32 v14, v71, v14
	v_add_f32_e32 v14, v72, v14
	v_add_f32_e32 v14, v73, v14
	v_cvt_pk_bf16_f32 v134, v68, v69
	v_cvt_pk_bf16_f32 v135, v70, v71
	ds_read_b64_tr_b16 v[88:89], v0 offset:27648
	ds_read_b64_tr_b16 v[90:91], v0 offset:28160
	s_waitcnt lgkmcnt(14)
	v_mfma_f32_32x32x16_bf16 v[112:127], v[164:167], v[144:147], v[112:127]
	v_add_f32_e32 v14, v74, v14
	v_add_f32_e32 v14, v75, v14
	v_add_f32_e32 v14, v76, v14
	v_add_f32_e32 v14, v77, v14
	v_cvt_pk_bf16_f32 v128, v72, v73
	v_cvt_pk_bf16_f32 v129, v74, v75
	ds_read_b64_tr_b16 v[92:93], v0 offset:31744
	ds_read_b64_tr_b16 v[94:95], v0 offset:32256
	v_mfma_f32_32x32x16_bf16 v[96:111], v[160:163], v[144:147], v[96:111]
	v_add_f32_e32 v0, v78, v14
	v_add_f32_e32 v0, v79, v0
	v_cvt_pk_bf16_f32 v130, v76, v77
	v_cvt_pk_bf16_f32 v131, v78, v79
.Lna_D_0:
	s_mov_b32 s44, m0
	s_mov_b32 m0, s27
	s_nop 0
	global_load_lds_dwordx4 v[198:199], off
	s_mov_b32 m0, s44
	s_andn2_b64 vcc, exec, s[42:43]
	s_mov_b64 s[44:45], -1
	s_cbranch_vccz .LBB0_532
	s_add_i32 s68, s23, s1
	s_lshl_b64 s[42:43], s[68:69], 6
	s_add_u32 s42, s42, s33
	s_addc_u32 s43, s43, 0
	s_mov_b64 s[44:45], 0

.Lna_Bm_0:
	s_cmp_lg_u32 s101, 0
	s_cbranch_scc1 .Lna_B3_0
	s_waitcnt lgkmcnt(14)
	v_mfma_f32_32x32x16_bf16 v[32:47], v[140:143], v[192:195], v[32:47]
	s_waitcnt lgkmcnt(12)
	v_mfma_f32_32x32x16_bf16 v[16:31], v[140:143], v[10:13], v[16:31]
	v_add_u32_e32 v14, s47, v227
	ds_read_b128 v[64:67], v14
	ds_read_b128 v[180:183], v14 offset:512
	s_waitcnt lgkmcnt(12)
	v_mfma_f32_32x32x16_bf16 v[32:47], v[136:139], v[2:5], v[32:47]
	ds_read_b128 v[184:187], v14 offset:2048
	ds_read_b128 v[10:13], v14 offset:2560
	s_waitcnt lgkmcnt(12)
	v_mfma_f32_32x32x16_bf16 v[16:31], v[136:139], v[6:9], v[16:31]
	ds_read_b128 v[176:179], v14 offset:4096
	ds_read_b128 v[172:175], v14 offset:4608
	s_waitcnt lgkmcnt(12)
	v_mfma_f32_32x32x16_bf16 v[32:47], v[132:135], v[80:83], v[32:47]
	ds_read_b128 v[168:171], v14 offset:6144
	ds_read_b128 v[164:167], v14 offset:6656
	s_waitcnt lgkmcnt(12)
	v_mfma_f32_32x32x16_bf16 v[16:31], v[132:135], v[84:87], v[16:31]
	s_waitcnt lgkmcnt(10)
	v_mfma_f32_32x32x16_bf16 v[32:47], v[128:131], v[88:91], v[32:47]
	s_waitcnt lgkmcnt(8)
	v_mfma_f32_32x32x16_bf16 v[16:31], v[128:131], v[92:95], v[16:31]
	s_branch .Lna_Bend_0
.Lna_B3_0:
	s_waitcnt lgkmcnt(14)
	s_waitcnt lgkmcnt(12)
	v_add_u32_e32 v14, s47, v227
	ds_read_b128 v[64:67], v14
	ds_read_b128 v[180:183], v14 offset:512
	s_waitcnt lgkmcnt(12)
	ds_read_b128 v[184:187], v14 offset:2048
	ds_read_b128 v[10:13], v14 offset:2560
	s_waitcnt lgkmcnt(12)
	ds_read_b128 v[176:179], v14 offset:4096
	ds_read_b128 v[172:175], v14 offset:4608
	s_waitcnt lgkmcnt(12)
	ds_read_b128 v[168:171], v14 offset:6144
	ds_read_b128 v[164:167], v14 offset:6656
	s_waitcnt lgkmcnt(12)
	s_waitcnt lgkmcnt(10)
	s_waitcnt lgkmcnt(8)
	s_branch .Lna_Bend_0
.Lna_B1_0:
	s_waitcnt lgkmcnt(14)
	v_exp_f32_e32 v112, v112
	v_exp_f32_e32 v113, v113
	v_exp_f32_e32 v114, v114
	v_exp_f32_e32 v115, v115
	s_waitcnt lgkmcnt(12)
	v_exp_f32_e32 v116, v116
	v_exp_f32_e32 v117, v117
	v_exp_f32_e32 v118, v118
	v_exp_f32_e32 v119, v119
	v_add_u32_e32 v14, s47, v227
	ds_read_b128 v[64:67], v14
	ds_read_b128 v[180:183], v14 offset:512
	s_waitcnt lgkmcnt(12)
	v_exp_f32_e32 v120, v120
	v_exp_f32_e32 v121, v121
	v_exp_f32_e32 v122, v122
	v_exp_f32_e32 v123, v123
	ds_read_b128 v[184:187], v14 offset:2048
	ds_read_b128 v[10:13], v14 offset:2560
	s_waitcnt lgkmcnt(12)
	v_exp_f32_e32 v124, v124
	v_exp_f32_e32 v125, v125
	v_exp_f32_e32 v126, v126
	v_exp_f32_e32 v127, v127
	ds_read_b128 v[176:179], v14 offset:4096
	ds_read_b128 v[172:175], v14 offset:4608
	s_waitcnt lgkmcnt(12)
	v_exp_f32_e32 v96, v96
	v_exp_f32_e32 v97, v97
	v_exp_f32_e32 v98, v98
	v_exp_f32_e32 v99, v99
	ds_read_b128 v[168:171], v14 offset:6144
	ds_read_b128 v[164:167], v14 offset:6656
	s_waitcnt lgkmcnt(12)
	v_exp_f32_e32 v100, v100
	v_exp_f32_e32 v101, v101
	v_exp_f32_e32 v102, v102
	v_exp_f32_e32 v103, v103
	s_waitcnt lgkmcnt(10)
	v_exp_f32_e32 v104, v104
	v_exp_f32_e32 v105, v105
	v_exp_f32_e32 v106, v106
	v_exp_f32_e32 v107, v107
	s_waitcnt lgkmcnt(8)
	v_exp_f32_e32 v108, v108
	v_exp_f32_e32 v109, v109
	v_exp_f32_e32 v110, v110
	v_exp_f32_e32 v111, v111
	s_branch .Lna_Bend_0
.Lna_skA_0:
	v_add_u32_e32 v0, s44, v226
	ds_read_b64_tr_b16 v[192:193], v0 offset:24576
	ds_read_b64_tr_b16 v[194:195], v0 offset:25088
	s_waitcnt lgkmcnt(9)
	v_add_f32_e32 v2, v80, v81
	v_add_f32_e32 v2, v82, v2
	v_add_f32_e32 v2, v83, v2
	v_add_f32_e32 v2, v84, v2
	v_add_f32_e32 v2, v85, v2
	v_cvt_pk_bf16_f32 v140, v80, v81
	v_cvt_pk_bf16_f32 v141, v82, v83
	ds_read_b64_tr_b16 v[10:11], v0 offset:28672
	ds_read_b64_tr_b16 v[12:13], v0 offset:29184
	s_waitcnt lgkmcnt(10)
	v_add_f32_e32 v2, v86, v2
	v_add_f32_e32 v2, v87, v2
	v_add_f32_e32 v2, v88, v2
	v_add_f32_e32 v6, v89, v2
	v_cvt_pk_bf16_f32 v142, v84, v85
	v_cvt_pk_bf16_f32 v143, v86, v87
	ds_read_b64_tr_b16 v[2:3], v0 offset:25600
	ds_read_b64_tr_b16 v[4:5], v0 offset:26112
	s_waitcnt lgkmcnt(11)
	v_add_f32_e32 v6, v90, v6
	v_add_f32_e32 v6, v91, v6
	v_add_f32_e32 v6, v92, v6
	v_add_f32_e32 v14, v93, v6
	v_cvt_pk_bf16_f32 v136, v88, v89
	v_cvt_pk_bf16_f32 v137, v90, v91
	ds_read_b64_tr_b16 v[6:7], v0 offset:29696
	ds_read_b64_tr_b16 v[8:9], v0 offset:30208
	s_waitcnt lgkmcnt(12)
	v_add_f32_e32 v14, v94, v14
	v_add_f32_e32 v14, v95, v14
	v_add_f32_e32 v14, v64, v14
	v_add_f32_e32 v14, v65, v14
	v_cvt_pk_bf16_f32 v138, v92, v93
	v_cvt_pk_bf16_f32 v139, v94, v95
	ds_read_b64_tr_b16 v[80:81], v0 offset:26624
	ds_read_b64_tr_b16 v[82:83], v0 offset:27136
	s_waitcnt lgkmcnt(13)
	v_add_f32_e32 v14, v66, v14
	v_add_f32_e32 v14, v67, v14
	v_add_f32_e32 v14, v68, v14
	v_add_f32_e32 v14, v69, v14
	v_cvt_pk_bf16_f32 v132, v64, v65
	v_cvt_pk_bf16_f32 v133, v66, v67
	ds_read_b64_tr_b16 v[84:85], v0 offset:30720
	ds_read_b64_tr_b16 v[86:87], v0 offset:31232
	s_waitcnt lgkmcnt(14)
	v_add_f32_e32 v14, v70, v14
	v_add_f32_e32 v14, v71, v14
	v_add_f32_e32 v14, v72, v14
	v_add_f32_e32 v14, v73, v14
	v_cvt_pk_bf16_f32 v134, v68, v69
	v_cvt_pk_bf16_f32 v135, v70, v71
	ds_read_b64_tr_b16 v[88:89], v0 offset:27648
	ds_read_b64_tr_b16 v[90:91], v0 offset:28160
	s_waitcnt lgkmcnt(14)
	v_add_f32_e32 v14, v74, v14
	v_add_f32_e32 v14, v75, v14
	v_add_f32_e32 v14, v76, v14
	v_add_f32_e32 v14, v77, v14
	v_cvt_pk_bf16_f32 v128, v72, v73
	v_cvt_pk_bf16_f32 v129, v74, v75
	ds_read_b64_tr_b16 v[92:93], v0 offset:31744
	ds_read_b64_tr_b16 v[94:95], v0 offset:32256
	v_add_f32_e32 v0, v78, v14
	v_add_f32_e32 v0, v79, v0
	v_cvt_pk_bf16_f32 v130, v76, v77
	v_cvt_pk_bf16_f32 v131, v78, v79
	s_branch .Lna_D_0
.Lna_allmask_0:
	v_mov_b32_e32 v112, 0
	v_mov_b32_e32 v113, 0
	v_mov_b32_e32 v114, 0
	v_mov_b32_e32 v115, 0
	v_mov_b32_e32 v116, 0
	v_mov_b32_e32 v117, 0
	v_mov_b32_e32 v118, 0
	v_mov_b32_e32 v119, 0
	v_mov_b32_e32 v120, 0
	v_mov_b32_e32 v121, 0
	v_mov_b32_e32 v122, 0
	v_mov_b32_e32 v123, 0
	v_mov_b32_e32 v124, 0
	v_mov_b32_e32 v125, 0
	v_mov_b32_e32 v126, 0
	v_mov_b32_e32 v127, 0
	v_mov_b32_e32 v96, 0
	v_mov_b32_e32 v97, 0
	v_mov_b32_e32 v98, 0
	v_mov_b32_e32 v99, 0
	v_mov_b32_e32 v100, 0
	v_mov_b32_e32 v101, 0
	v_mov_b32_e32 v102, 0
	v_mov_b32_e32 v103, 0
	v_mov_b32_e32 v104, 0
	v_mov_b32_e32 v105, 0
	v_mov_b32_e32 v106, 0
	v_mov_b32_e32 v107, 0
	v_mov_b32_e32 v108, 0
	v_mov_b32_e32 v109, 0
	v_mov_b32_e32 v110, 0
	v_mov_b32_e32 v111, 0

.LBB0_569:
	s_cmp_lg_u32 s100, 0
	s_cbranch_scc1 .Lna_Bm_0
	s_cmp_lg_u32 s101, 0
	s_cbranch_scc1 .Lna_B1_0
	s_waitcnt lgkmcnt(14)
	v_mfma_f32_32x32x16_bf16 v[32:47], v[140:143], v[192:195], v[32:47]
	v_exp_f32_e32 v112, v112
	v_exp_f32_e32 v113, v113
	v_exp_f32_e32 v114, v114
	v_exp_f32_e32 v115, v115
	s_waitcnt lgkmcnt(12)
	v_mfma_f32_32x32x16_bf16 v[16:31], v[140:143], v[10:13], v[16:31]
	v_exp_f32_e32 v116, v116
	v_exp_f32_e32 v117, v117
	v_exp_f32_e32 v118, v118
	v_exp_f32_e32 v119, v119
	v_add_u32_e32 v14, s47, v227
	ds_read_b128 v[64:67], v14
	ds_read_b128 v[180:183], v14 offset:512
	s_waitcnt lgkmcnt(12)
	v_mfma_f32_32x32x16_bf16 v[32:47], v[136:139], v[2:5], v[32:47]
	v_exp_f32_e32 v120, v120
	v_exp_f32_e32 v121, v121
	v_exp_f32_e32 v122, v122
	v_exp_f32_e32 v123, v123
	ds_read_b128 v[184:187], v14 offset:2048
	ds_read_b128 v[10:13], v14 offset:2560
	s_waitcnt lgkmcnt(12)
	v_mfma_f32_32x32x16_bf16 v[16:31], v[136:139], v[6:9], v[16:31]
	v_exp_f32_e32 v124, v124
	v_exp_f32_e32 v125, v125
	v_exp_f32_e32 v126, v126
	v_exp_f32_e32 v127, v127
	ds_read_b128 v[176:179], v14 offset:4096
	ds_read_b128 v[172:175], v14 offset:4608
	s_waitcnt lgkmcnt(12)
	v_mfma_f32_32x32x16_bf16 v[32:47], v[132:135], v[80:83], v[32:47]
	v_exp_f32_e32 v96, v96
	v_exp_f32_e32 v97, v97
	v_exp_f32_e32 v98, v98
	v_exp_f32_e32 v99, v99
	ds_read_b128 v[168:171], v14 offset:6144
	ds_read_b128 v[164:167], v14 offset:6656
	s_waitcnt lgkmcnt(12)
	v_mfma_f32_32x32x16_bf16 v[16:31], v[132:135], v[84:87], v[16:31]
	v_exp_f32_e32 v100, v100
	v_exp_f32_e32 v101, v101
	v_exp_f32_e32 v102, v102
	v_exp_f32_e32 v103, v103
	s_waitcnt lgkmcnt(10)
	v_mfma_f32_32x32x16_bf16 v[32:47], v[128:131], v[88:91], v[32:47]
	v_exp_f32_e32 v104, v104
	v_exp_f32_e32 v105, v105
	v_exp_f32_e32 v106, v106
	v_exp_f32_e32 v107, v107
	s_waitcnt lgkmcnt(8)
	v_mfma_f32_32x32x16_bf16 v[16:31], v[128:131], v[92:95], v[16:31]
	v_exp_f32_e32 v108, v108
	v_exp_f32_e32 v109, v109
	v_exp_f32_e32 v110, v110
	v_exp_f32_e32 v111, v111
.Lna_Bend_0:
	s_waitcnt vmcnt(2) lgkmcnt(0)
	s_barrier
	s_andn2_b64 vcc, exec, s[42:43]
	s_cbranch_vccnz .LBB0_571
	s_waitcnt lgkmcnt(0)
	ds_read_b128 v[2:5], v220 offset:49248
	ds_read_b128 v[6:9], v220 offset:49216
	ds_read_b128 v[68:71], v220 offset:49184
	ds_read_b128 v[72:75], v220 offset:49152
	s_waitcnt lgkmcnt(3)
	v_pk_mul_f32 v[46:47], v[46:47], v[4:5]
	s_waitcnt lgkmcnt(2)
	v_pk_mul_f32 v[42:43], v[42:43], v[8:9]
	s_waitcnt lgkmcnt(1)
	v_pk_mul_f32 v[38:39], v[38:39], v[70:71]
	s_waitcnt lgkmcnt(0)
	v_pk_mul_f32 v[34:35], v[34:35], v[74:75]
	v_pk_mul_f32 v[44:45], v[44:45], v[2:3]
	v_pk_mul_f32 v[40:41], v[40:41], v[6:7]
	v_pk_mul_f32 v[36:37], v[36:37], v[68:69]
	v_pk_mul_f32 v[32:33], v[32:33], v[72:73]
	v_pk_mul_f32 v[30:31], v[30:31], v[4:5]
	v_pk_mul_f32 v[26:27], v[26:27], v[8:9]
	v_pk_mul_f32 v[22:23], v[22:23], v[70:71]
	v_pk_mul_f32 v[18:19], v[18:19], v[74:75]
	v_pk_mul_f32 v[28:29], v[28:29], v[2:3]
	v_pk_mul_f32 v[24:25], v[24:25], v[6:7]
	v_pk_mul_f32 v[20:21], v[20:21], v[68:69]
	v_pk_mul_f32 v[16:17], v[16:17], v[72:73]
.LBB0_571:
	s_mov_b32 s101, s100
	s_mov_b32 s100, 0
	s_cmp_lt_u32 s26, 3
	s_cbranch_scc1 .Lna_ent_1
	s_add_i32 vcc_lo, s50, s23
	s_add_i32 vcc_lo, vcc_lo, -4
	s_cmp_gt_u32 vcc_lo, 7
	s_cselect_b32 s100, 1, 0
	s_cbranch_scc1 .Lna_skA_1

.Lna_D_1:
	s_mov_b64 s[42:43], 0xd8000
	v_lshl_add_u64 v[96:97], v[198:199], 0, s[42:43]
	s_add_i32 s27, s47, s8
	s_mov_b32 s42, m0
	s_mov_b32 m0, s27
	s_nop 0
	global_load_lds_dwordx4 v[96:97], off
	s_mov_b32 m0, s42
	s_cmp_lt_u32 s26, 2
	s_mov_b64 s[42:43], s[6:7]
	s_cbranch_scc1 .LBB0_573
	s_add_i32 s27, s23, s1
	s_add_i32 s68, s27, 1
	s_lshl_b64 s[42:43], s[68:69], 6
	s_add_u32 s42, s42, s33
	s_addc_u32 s43, s43, 0

.Lna_Bm_1:
	s_cmp_lg_u32 s101, 0
	s_cbranch_scc1 .Lna_B3_1
	s_waitcnt lgkmcnt(14)
	v_mfma_f32_32x32x16_bf16 v[32:47], v[140:143], v[160:163], v[32:47]
	s_waitcnt lgkmcnt(12)
	v_mfma_f32_32x32x16_bf16 v[16:31], v[140:143], v[112:115], v[16:31]
	v_add_u32_e32 v0, s64, v227
	ds_read_b128 v[188:191], v0
	ds_read_b128 v[184:187], v0 offset:512
	s_waitcnt lgkmcnt(12)
	v_mfma_f32_32x32x16_bf16 v[32:47], v[136:139], v[2:5], v[32:47]
	ds_read_b128 v[180:183], v0 offset:2048
	ds_read_b128 v[176:179], v0 offset:2560
	s_waitcnt lgkmcnt(12)
	v_mfma_f32_32x32x16_bf16 v[16:31], v[136:139], v[6:9], v[16:31]
	ds_read_b128 v[172:175], v0 offset:4096
	ds_read_b128 v[168:171], v0 offset:4608
	s_waitcnt lgkmcnt(12)
	v_mfma_f32_32x32x16_bf16 v[32:47], v[132:135], v[10:13], v[32:47]
	ds_read_b128 v[164:167], v0 offset:6144
	ds_read_b128 v[160:163], v0 offset:6656
	s_waitcnt lgkmcnt(12)
	v_mfma_f32_32x32x16_bf16 v[16:31], v[132:135], v[116:119], v[16:31]
	s_waitcnt lgkmcnt(10)
	v_mfma_f32_32x32x16_bf16 v[32:47], v[128:131], v[120:123], v[32:47]
	s_waitcnt lgkmcnt(8)
	v_mfma_f32_32x32x16_bf16 v[16:31], v[128:131], v[124:127], v[16:31]
	s_branch .Lna_Bend_1
.Lna_B3_1:
	s_waitcnt lgkmcnt(14)
	s_waitcnt lgkmcnt(12)
	v_add_u32_e32 v0, s64, v227
	ds_read_b128 v[188:191], v0
	ds_read_b128 v[184:187], v0 offset:512
	s_waitcnt lgkmcnt(12)
	ds_read_b128 v[180:183], v0 offset:2048
	ds_read_b128 v[176:179], v0 offset:2560
	s_waitcnt lgkmcnt(12)
	ds_read_b128 v[172:175], v0 offset:4096
	ds_read_b128 v[168:171], v0 offset:4608
	s_waitcnt lgkmcnt(12)
	ds_read_b128 v[164:167], v0 offset:6144
	ds_read_b128 v[160:163], v0 offset:6656
	s_waitcnt lgkmcnt(12)
	s_waitcnt lgkmcnt(10)
	s_waitcnt lgkmcnt(8)
	s_branch .Lna_Bend_1
.Lna_B1_1:
	s_waitcnt lgkmcnt(14)
	v_exp_f32_e32 v80, v80
	v_exp_f32_e32 v81, v81
	v_exp_f32_e32 v82, v82
	v_exp_f32_e32 v83, v83
	s_waitcnt lgkmcnt(12)
	v_exp_f32_e32 v84, v84
	v_exp_f32_e32 v85, v85
	v_exp_f32_e32 v86, v86
	v_exp_f32_e32 v87, v87
	v_add_u32_e32 v0, s64, v227
	ds_read_b128 v[188:191], v0
	ds_read_b128 v[184:187], v0 offset:512
	s_waitcnt lgkmcnt(12)
	v_exp_f32_e32 v88, v88
	v_exp_f32_e32 v89, v89
	v_exp_f32_e32 v90, v90
	v_exp_f32_e32 v91, v91
	ds_read_b128 v[180:183], v0 offset:2048
	ds_read_b128 v[176:179], v0 offset:2560
	s_waitcnt lgkmcnt(12)
	v_exp_f32_e32 v92, v92
	v_exp_f32_e32 v93, v93
	v_exp_f32_e32 v94, v94
	v_exp_f32_e32 v95, v95
	ds_read_b128 v[172:175], v0 offset:4096
	ds_read_b128 v[168:171], v0 offset:4608
	s_waitcnt lgkmcnt(12)
	v_exp_f32_e32 v64, v64
	v_exp_f32_e32 v65, v65
	v_exp_f32_e32 v66, v66
	v_exp_f32_e32 v67, v67
	ds_read_b128 v[164:167], v0 offset:6144
	ds_read_b128 v[160:163], v0 offset:6656
	s_waitcnt lgkmcnt(12)
	v_exp_f32_e32 v68, v68
	v_exp_f32_e32 v69, v69
	v_exp_f32_e32 v70, v70
	v_exp_f32_e32 v71, v71
	s_waitcnt lgkmcnt(10)
	v_exp_f32_e32 v72, v72
	v_exp_f32_e32 v73, v73
	v_exp_f32_e32 v74, v74
	v_exp_f32_e32 v75, v75
	s_waitcnt lgkmcnt(8)
	v_exp_f32_e32 v76, v76
	v_exp_f32_e32 v77, v77
	v_exp_f32_e32 v78, v78
	v_exp_f32_e32 v79, v79
	s_branch .Lna_Bend_1
.Lna_skA_1:
	v_add_u32_e32 v14, s64, v226
	ds_read_b64_tr_b16 v[160:161], v14 offset:24576
	ds_read_b64_tr_b16 v[162:163], v14 offset:25088
	s_waitcnt lgkmcnt(9)
	v_add_f32_e32 v2, v112, v113
	v_add_f32_e32 v2, v114, v2
	v_add_f32_e32 v2, v115, v2
	v_add_f32_e32 v2, v116, v2
	v_add_f32_e32 v2, v117, v2
	v_cvt_pk_bf16_f32 v140, v112, v113
	v_cvt_pk_bf16_f32 v141, v114, v115
	ds_read_b64_tr_b16 v[112:113], v14 offset:28672
	ds_read_b64_tr_b16 v[114:115], v14 offset:29184
	s_waitcnt lgkmcnt(10)
	v_add_f32_e32 v2, v118, v2
	v_add_f32_e32 v2, v119, v2
	v_add_f32_e32 v2, v120, v2
	v_add_f32_e32 v6, v121, v2
	v_cvt_pk_bf16_f32 v142, v116, v117
	v_cvt_pk_bf16_f32 v143, v118, v119
	ds_read_b64_tr_b16 v[2:3], v14 offset:25600
	ds_read_b64_tr_b16 v[4:5], v14 offset:26112
	s_waitcnt lgkmcnt(11)
	v_add_f32_e32 v6, v122, v6
	v_add_f32_e32 v6, v123, v6
	v_add_f32_e32 v6, v124, v6
	v_add_f32_e32 v15, v125, v6
	v_cvt_pk_bf16_f32 v136, v120, v121
	v_cvt_pk_bf16_f32 v137, v122, v123
	ds_read_b64_tr_b16 v[6:7], v14 offset:29696
	ds_read_b64_tr_b16 v[8:9], v14 offset:30208
	s_waitcnt lgkmcnt(12)
	v_add_f32_e32 v10, v126, v15
	v_add_f32_e32 v10, v127, v10
	v_add_f32_e32 v10, v96, v10
	v_add_f32_e32 v15, v97, v10
	v_cvt_pk_bf16_f32 v138, v124, v125
	v_cvt_pk_bf16_f32 v139, v126, v127
	ds_read_b64_tr_b16 v[10:11], v14 offset:26624
	ds_read_b64_tr_b16 v[12:13], v14 offset:27136
	s_waitcnt lgkmcnt(13)
	v_add_f32_e32 v15, v98, v15
	v_add_f32_e32 v15, v99, v15
	v_add_f32_e32 v15, v100, v15
	v_add_f32_e32 v15, v101, v15
	v_cvt_pk_bf16_f32 v132, v96, v97
	v_cvt_pk_bf16_f32 v133, v98, v99
	ds_read_b64_tr_b16 v[116:117], v14 offset:30720
	ds_read_b64_tr_b16 v[118:119], v14 offset:31232
	s_waitcnt lgkmcnt(14)
	v_add_f32_e32 v15, v102, v15
	v_add_f32_e32 v15, v103, v15
	v_add_f32_e32 v15, v104, v15
	v_add_f32_e32 v15, v105, v15
	v_cvt_pk_bf16_f32 v134, v100, v101
	v_cvt_pk_bf16_f32 v135, v102, v103
	ds_read_b64_tr_b16 v[120:121], v14 offset:27648
	ds_read_b64_tr_b16 v[122:123], v14 offset:28160
	s_waitcnt lgkmcnt(14)
	v_add_f32_e32 v15, v106, v15
	v_add_f32_e32 v15, v107, v15
	v_add_f32_e32 v15, v108, v15
	v_add_f32_e32 v15, v109, v15
	v_cvt_pk_bf16_f32 v128, v104, v105
	v_cvt_pk_bf16_f32 v129, v106, v107
	ds_read_b64_tr_b16 v[124:125], v14 offset:31744
	ds_read_b64_tr_b16 v[126:127], v14 offset:32256
	v_add_f32_e32 v14, v110, v15
	v_add_f32_e32 v14, v111, v14
	v_cvt_pk_bf16_f32 v130, v108, v109
	v_cvt_pk_bf16_f32 v131, v110, v111
	s_branch .Lna_D_1
.Lna_allmask_1:
	v_mov_b32_e32 v80, 0
	v_mov_b32_e32 v81, 0
	v_mov_b32_e32 v82, 0
	v_mov_b32_e32 v83, 0
	v_mov_b32_e32 v84, 0
	v_mov_b32_e32 v85, 0
	v_mov_b32_e32 v86, 0
	v_mov_b32_e32 v87, 0
	v_mov_b32_e32 v88, 0
	v_mov_b32_e32 v89, 0
	v_mov_b32_e32 v90, 0
	v_mov_b32_e32 v91, 0
	v_mov_b32_e32 v92, 0
	v_mov_b32_e32 v93, 0
	v_mov_b32_e32 v94, 0
	v_mov_b32_e32 v95, 0
	v_mov_b32_e32 v64, 0
	v_mov_b32_e32 v65, 0
	v_mov_b32_e32 v66, 0
	v_mov_b32_e32 v67, 0
	v_mov_b32_e32 v68, 0
	v_mov_b32_e32 v69, 0
	v_mov_b32_e32 v70, 0
	v_mov_b32_e32 v71, 0
	v_mov_b32_e32 v72, 0
	v_mov_b32_e32 v73, 0
	v_mov_b32_e32 v74, 0
	v_mov_b32_e32 v75, 0
	v_mov_b32_e32 v76, 0
	v_mov_b32_e32 v77, 0
	v_mov_b32_e32 v78, 0
	v_mov_b32_e32 v79, 0

.LBB0_608:
	s_cmp_lg_u32 s100, 0
	s_cbranch_scc1 .Lna_Bm_1
	s_cmp_lg_u32 s101, 0
	s_cbranch_scc1 .Lna_B1_1
	s_waitcnt lgkmcnt(14)
	v_mfma_f32_32x32x16_bf16 v[32:47], v[140:143], v[160:163], v[32:47]
	v_exp_f32_e32 v80, v80
	v_exp_f32_e32 v81, v81
	v_exp_f32_e32 v82, v82
	v_exp_f32_e32 v83, v83
	s_waitcnt lgkmcnt(12)
	v_mfma_f32_32x32x16_bf16 v[16:31], v[140:143], v[112:115], v[16:31]
	v_exp_f32_e32 v84, v84
	v_exp_f32_e32 v85, v85
	v_exp_f32_e32 v86, v86
	v_exp_f32_e32 v87, v87
	v_add_u32_e32 v0, s64, v227
	ds_read_b128 v[188:191], v0
	ds_read_b128 v[184:187], v0 offset:512
	s_waitcnt lgkmcnt(12)
	v_mfma_f32_32x32x16_bf16 v[32:47], v[136:139], v[2:5], v[32:47]
	v_exp_f32_e32 v88, v88
	v_exp_f32_e32 v89, v89
	v_exp_f32_e32 v90, v90
	v_exp_f32_e32 v91, v91
	ds_read_b128 v[180:183], v0 offset:2048
	ds_read_b128 v[176:179], v0 offset:2560
	s_waitcnt lgkmcnt(12)
	v_mfma_f32_32x32x16_bf16 v[16:31], v[136:139], v[6:9], v[16:31]
	v_exp_f32_e32 v92, v92
	v_exp_f32_e32 v93, v93
	v_exp_f32_e32 v94, v94
	v_exp_f32_e32 v95, v95
	ds_read_b128 v[172:175], v0 offset:4096
	ds_read_b128 v[168:171], v0 offset:4608
	s_waitcnt lgkmcnt(12)
	v_mfma_f32_32x32x16_bf16 v[32:47], v[132:135], v[10:13], v[32:47]
	v_exp_f32_e32 v64, v64
	v_exp_f32_e32 v65, v65
	v_exp_f32_e32 v66, v66
	v_exp_f32_e32 v67, v67
	ds_read_b128 v[164:167], v0 offset:6144
	ds_read_b128 v[160:163], v0 offset:6656
	s_waitcnt lgkmcnt(12)
	v_mfma_f32_32x32x16_bf16 v[16:31], v[132:135], v[116:119], v[16:31]
	v_exp_f32_e32 v68, v68
	v_exp_f32_e32 v69, v69
	v_exp_f32_e32 v70, v70
	v_exp_f32_e32 v71, v71
	s_waitcnt lgkmcnt(10)
	v_mfma_f32_32x32x16_bf16 v[32:47], v[128:131], v[120:123], v[32:47]
	v_exp_f32_e32 v72, v72
	v_exp_f32_e32 v73, v73
	v_exp_f32_e32 v74, v74
	v_exp_f32_e32 v75, v75
	s_waitcnt lgkmcnt(8)
	v_mfma_f32_32x32x16_bf16 v[16:31], v[128:131], v[124:127], v[16:31]
	v_exp_f32_e32 v76, v76
	v_exp_f32_e32 v77, v77
	v_exp_f32_e32 v78, v78
	v_exp_f32_e32 v79, v79
.Lna_Bend_1:
	s_waitcnt vmcnt(2) lgkmcnt(0)
	s_barrier
	s_andn2_b64 vcc, exec, s[42:43]
	s_cbranch_vccnz .LBB0_610
	s_waitcnt lgkmcnt(0)
	ds_read_b128 v[2:5], v220 offset:49248
	ds_read_b128 v[6:9], v220 offset:49216
	ds_read_b128 v[10:13], v220 offset:49184
	ds_read_b128 v[96:99], v220 offset:49152
	s_waitcnt lgkmcnt(3)
	v_pk_mul_f32 v[46:47], v[46:47], v[4:5]
	s_waitcnt lgkmcnt(2)
	v_pk_mul_f32 v[42:43], v[42:43], v[8:9]
	s_waitcnt lgkmcnt(1)
	v_pk_mul_f32 v[38:39], v[38:39], v[12:13]
	s_waitcnt lgkmcnt(0)
	v_pk_mul_f32 v[34:35], v[34:35], v[98:99]
	v_pk_mul_f32 v[44:45], v[44:45], v[2:3]
	v_pk_mul_f32 v[40:41], v[40:41], v[6:7]
	v_pk_mul_f32 v[36:37], v[36:37], v[10:11]
	v_pk_mul_f32 v[32:33], v[32:33], v[96:97]
	v_pk_mul_f32 v[30:31], v[30:31], v[4:5]
	v_pk_mul_f32 v[26:27], v[26:27], v[8:9]
	v_pk_mul_f32 v[22:23], v[22:23], v[12:13]
	v_pk_mul_f32 v[18:19], v[18:19], v[98:99]
	v_pk_mul_f32 v[28:29], v[28:29], v[2:3]
	v_pk_mul_f32 v[24:25], v[24:25], v[6:7]
	v_pk_mul_f32 v[20:21], v[20:21], v[10:11]
	v_pk_mul_f32 v[16:17], v[16:17], v[96:97]

.LBB0_621:
	s_add_i32 s50, s23, s75
	s_mov_b32 s101, s100
	s_mov_b32 s100, 0
	s_cmp_lt_u32 s50, 4
	s_cbranch_scc1 .Lna_ent_2
	s_add_i32 vcc_lo, s23, s90
	s_add_i32 vcc_lo, vcc_lo, -8
	s_cmp_gt_u32 vcc_lo, 7
	s_cselect_b32 s100, 1, 0
	s_cbranch_scc1 .Lna_skA_2
.Lna_ent_2:
	v_add_u32_e32 v0, s47, v226
	ds_read_b64_tr_b16 v[192:193], v0 offset:24576
	ds_read_b64_tr_b16 v[194:195], v0 offset:25088
	s_waitcnt lgkmcnt(9)
	v_mfma_f32_32x32x16_bf16 v[112:127], v[188:191], v[156:159], v[48:63]
	v_add_f32_e32 v2, v80, v81
	v_add_f32_e32 v2, v82, v2
	v_add_f32_e32 v2, v83, v2
	v_add_f32_e32 v2, v84, v2
	v_add_f32_e32 v2, v85, v2
	v_cvt_pk_bf16_f32 v140, v80, v81
	v_cvt_pk_bf16_f32 v141, v82, v83
	ds_read_b64_tr_b16 v[80:81], v0 offset:28672
	ds_read_b64_tr_b16 v[82:83], v0 offset:29184
	s_waitcnt lgkmcnt(10)
	v_mfma_f32_32x32x16_bf16 v[96:111], v[184:187], v[156:159], v[48:63]
	v_add_f32_e32 v2, v86, v2
	v_add_f32_e32 v2, v87, v2
	v_add_f32_e32 v2, v88, v2
	v_add_f32_e32 v6, v89, v2
	v_cvt_pk_bf16_f32 v142, v84, v85
	v_cvt_pk_bf16_f32 v143, v86, v87
	ds_read_b64_tr_b16 v[2:3], v0 offset:25600
	ds_read_b64_tr_b16 v[4:5], v0 offset:26112
	s_waitcnt lgkmcnt(11)
	v_mfma_f32_32x32x16_bf16 v[112:127], v[180:183], v[152:155], v[112:127]
	v_add_f32_e32 v6, v90, v6
	v_add_f32_e32 v6, v91, v6
	v_add_f32_e32 v6, v92, v6
	v_add_f32_e32 v10, v93, v6
	v_cvt_pk_bf16_f32 v136, v88, v89
	v_cvt_pk_bf16_f32 v137, v90, v91
	ds_read_b64_tr_b16 v[6:7], v0 offset:29696
	ds_read_b64_tr_b16 v[8:9], v0 offset:30208
	s_waitcnt lgkmcnt(12)
	v_mfma_f32_32x32x16_bf16 v[96:111], v[176:179], v[152:155], v[96:111]
	v_add_f32_e32 v10, v94, v10
	v_add_f32_e32 v10, v95, v10
	v_add_f32_e32 v10, v64, v10
	v_add_f32_e32 v84, v65, v10
	v_cvt_pk_bf16_f32 v138, v92, v93
	v_cvt_pk_bf16_f32 v139, v94, v95
	ds_read_b64_tr_b16 v[10:11], v0 offset:26624
	ds_read_b64_tr_b16 v[12:13], v0 offset:27136
	s_waitcnt lgkmcnt(13)
	v_mfma_f32_32x32x16_bf16 v[112:127], v[172:175], v[148:151], v[112:127]
	v_add_f32_e32 v84, v66, v84
	v_add_f32_e32 v84, v67, v84
	v_add_f32_e32 v84, v68, v84
	v_add_f32_e32 v88, v69, v84
	v_cvt_pk_bf16_f32 v132, v64, v65
	v_cvt_pk_bf16_f32 v133, v66, v67
	ds_read_b64_tr_b16 v[84:85], v0 offset:30720
	ds_read_b64_tr_b16 v[86:87], v0 offset:31232
	s_waitcnt lgkmcnt(14)
	v_mfma_f32_32x32x16_bf16 v[96:111], v[168:171], v[148:151], v[96:111]
	v_add_f32_e32 v64, v70, v88
	v_add_f32_e32 v64, v71, v64
	v_add_f32_e32 v64, v72, v64
	v_add_f32_e32 v64, v73, v64
	v_cvt_pk_bf16_f32 v134, v68, v69
	v_cvt_pk_bf16_f32 v135, v70, v71
	ds_read_b64_tr_b16 v[88:89], v0 offset:27648
	ds_read_b64_tr_b16 v[90:91], v0 offset:28160
	s_waitcnt lgkmcnt(14)
	v_mfma_f32_32x32x16_bf16 v[112:127], v[164:167], v[144:147], v[112:127]
	v_add_f32_e32 v64, v74, v64
	v_add_f32_e32 v64, v75, v64
	v_add_f32_e32 v64, v76, v64
	v_add_f32_e32 v64, v77, v64
	v_cvt_pk_bf16_f32 v128, v72, v73
	v_cvt_pk_bf16_f32 v129, v74, v75
	ds_read_b64_tr_b16 v[92:93], v0 offset:31744
	ds_read_b64_tr_b16 v[94:95], v0 offset:32256
	v_mfma_f32_32x32x16_bf16 v[96:111], v[160:163], v[144:147], v[96:111]
	v_add_f32_e32 v0, v78, v64
	v_add_f32_e32 v0, v79, v0
	v_cvt_pk_bf16_f32 v130, v76, v77
	v_cvt_pk_bf16_f32 v131, v78, v79
.Lna_D_2:
	s_cmp_ge_i32 s50, s88
	s_cselect_b64 s[44:45], -1, 0
	s_and_b64 vcc, exec, s[44:45]
	s_cbranch_vccnz .LBB0_623
	s_add_i32 s6, s64, s8
	s_mov_b32 s7, m0
	s_mov_b32 m0, s6
	s_nop 0
	global_load_lds_dwordx4 v[206:207], off
	s_mov_b32 m0, s7

.Lna_Bm_2:
	s_cmp_lg_u32 s101, 0
	s_cbranch_scc1 .Lna_B3_2
	s_waitcnt lgkmcnt(14)
	v_mfma_f32_32x32x16_bf16 v[32:47], v[140:143], v[192:195], v[32:47]
	s_waitcnt lgkmcnt(12)
	v_mfma_f32_32x32x16_bf16 v[16:31], v[140:143], v[80:83], v[16:31]
	v_add_u32_e32 v64, s81, v227
	ds_read_b128 v[188:191], v64
	ds_read_b128 v[184:187], v64 offset:512
	s_waitcnt lgkmcnt(12)
	v_mfma_f32_32x32x16_bf16 v[32:47], v[136:139], v[2:5], v[32:47]
	ds_read_b128 v[180:183], v64 offset:2048
	ds_read_b128 v[176:179], v64 offset:2560
	s_waitcnt lgkmcnt(12)
	v_mfma_f32_32x32x16_bf16 v[16:31], v[136:139], v[6:9], v[16:31]
	ds_read_b128 v[172:175], v64 offset:4096
	ds_read_b128 v[168:171], v64 offset:4608
	s_waitcnt lgkmcnt(12)
	v_mfma_f32_32x32x16_bf16 v[32:47], v[132:135], v[10:13], v[32:47]
	ds_read_b128 v[164:167], v64 offset:6144
	ds_read_b128 v[160:163], v64 offset:6656
	s_waitcnt lgkmcnt(12)
	v_mfma_f32_32x32x16_bf16 v[16:31], v[132:135], v[84:87], v[16:31]
	s_waitcnt lgkmcnt(10)
	v_mfma_f32_32x32x16_bf16 v[32:47], v[128:131], v[88:91], v[32:47]
	s_waitcnt lgkmcnt(8)
	v_mfma_f32_32x32x16_bf16 v[16:31], v[128:131], v[92:95], v[16:31]
	s_branch .Lna_Bend_2
.Lna_B3_2:
	s_waitcnt lgkmcnt(14)
	s_waitcnt lgkmcnt(12)
	v_add_u32_e32 v64, s81, v227
	ds_read_b128 v[188:191], v64
	ds_read_b128 v[184:187], v64 offset:512
	s_waitcnt lgkmcnt(12)
	ds_read_b128 v[180:183], v64 offset:2048
	ds_read_b128 v[176:179], v64 offset:2560
	s_waitcnt lgkmcnt(12)
	ds_read_b128 v[172:175], v64 offset:4096
	ds_read_b128 v[168:171], v64 offset:4608
	s_waitcnt lgkmcnt(12)
	ds_read_b128 v[164:167], v64 offset:6144
	ds_read_b128 v[160:163], v64 offset:6656
	s_waitcnt lgkmcnt(12)
	s_waitcnt lgkmcnt(10)
	s_waitcnt lgkmcnt(8)
	s_branch .Lna_Bend_2
.Lna_B1_2:
	s_waitcnt lgkmcnt(14)
	v_exp_f32_e32 v112, v112
	v_exp_f32_e32 v113, v113
	v_exp_f32_e32 v114, v114
	v_exp_f32_e32 v115, v115
	s_waitcnt lgkmcnt(12)
	v_exp_f32_e32 v116, v116
	v_exp_f32_e32 v117, v117
	v_exp_f32_e32 v118, v118
	v_exp_f32_e32 v119, v119
	v_add_u32_e32 v64, s81, v227
	ds_read_b128 v[188:191], v64
	ds_read_b128 v[184:187], v64 offset:512
	s_waitcnt lgkmcnt(12)
	v_exp_f32_e32 v120, v120
	v_exp_f32_e32 v121, v121
	v_exp_f32_e32 v122, v122
	v_exp_f32_e32 v123, v123
	ds_read_b128 v[180:183], v64 offset:2048
	ds_read_b128 v[176:179], v64 offset:2560
	s_waitcnt lgkmcnt(12)
	v_exp_f32_e32 v124, v124
	v_exp_f32_e32 v125, v125
	v_exp_f32_e32 v126, v126
	v_exp_f32_e32 v127, v127
	ds_read_b128 v[172:175], v64 offset:4096
	ds_read_b128 v[168:171], v64 offset:4608
	s_waitcnt lgkmcnt(12)
	v_exp_f32_e32 v96, v96
	v_exp_f32_e32 v97, v97
	v_exp_f32_e32 v98, v98
	v_exp_f32_e32 v99, v99
	ds_read_b128 v[164:167], v64 offset:6144
	ds_read_b128 v[160:163], v64 offset:6656
	s_waitcnt lgkmcnt(12)
	v_exp_f32_e32 v100, v100
	v_exp_f32_e32 v101, v101
	v_exp_f32_e32 v102, v102
	v_exp_f32_e32 v103, v103
	s_waitcnt lgkmcnt(10)
	v_exp_f32_e32 v104, v104
	v_exp_f32_e32 v105, v105
	v_exp_f32_e32 v106, v106
	v_exp_f32_e32 v107, v107
	s_waitcnt lgkmcnt(8)
	v_exp_f32_e32 v108, v108
	v_exp_f32_e32 v109, v109
	v_exp_f32_e32 v110, v110
	v_exp_f32_e32 v111, v111
	s_branch .Lna_Bend_2
.Lna_skA_2:
	v_add_u32_e32 v0, s47, v226
	ds_read_b64_tr_b16 v[192:193], v0 offset:24576
	ds_read_b64_tr_b16 v[194:195], v0 offset:25088
	s_waitcnt lgkmcnt(9)
	v_add_f32_e32 v2, v80, v81
	v_add_f32_e32 v2, v82, v2
	v_add_f32_e32 v2, v83, v2
	v_add_f32_e32 v2, v84, v2
	v_add_f32_e32 v2, v85, v2
	v_cvt_pk_bf16_f32 v140, v80, v81
	v_cvt_pk_bf16_f32 v141, v82, v83
	ds_read_b64_tr_b16 v[80:81], v0 offset:28672
	ds_read_b64_tr_b16 v[82:83], v0 offset:29184
	s_waitcnt lgkmcnt(10)
	v_add_f32_e32 v2, v86, v2
	v_add_f32_e32 v2, v87, v2
	v_add_f32_e32 v2, v88, v2
	v_add_f32_e32 v6, v89, v2
	v_cvt_pk_bf16_f32 v142, v84, v85
	v_cvt_pk_bf16_f32 v143, v86, v87
	ds_read_b64_tr_b16 v[2:3], v0 offset:25600
	ds_read_b64_tr_b16 v[4:5], v0 offset:26112
	s_waitcnt lgkmcnt(11)
	v_add_f32_e32 v6, v90, v6
	v_add_f32_e32 v6, v91, v6
	v_add_f32_e32 v6, v92, v6
	v_add_f32_e32 v10, v93, v6
	v_cvt_pk_bf16_f32 v136, v88, v89
	v_cvt_pk_bf16_f32 v137, v90, v91
	ds_read_b64_tr_b16 v[6:7], v0 offset:29696
	ds_read_b64_tr_b16 v[8:9], v0 offset:30208
	s_waitcnt lgkmcnt(12)
	v_add_f32_e32 v10, v94, v10
	v_add_f32_e32 v10, v95, v10
	v_add_f32_e32 v10, v64, v10
	v_add_f32_e32 v84, v65, v10
	v_cvt_pk_bf16_f32 v138, v92, v93
	v_cvt_pk_bf16_f32 v139, v94, v95
	ds_read_b64_tr_b16 v[10:11], v0 offset:26624
	ds_read_b64_tr_b16 v[12:13], v0 offset:27136
	s_waitcnt lgkmcnt(13)
	v_add_f32_e32 v84, v66, v84
	v_add_f32_e32 v84, v67, v84
	v_add_f32_e32 v84, v68, v84
	v_add_f32_e32 v88, v69, v84
	v_cvt_pk_bf16_f32 v132, v64, v65
	v_cvt_pk_bf16_f32 v133, v66, v67
	ds_read_b64_tr_b16 v[84:85], v0 offset:30720
	ds_read_b64_tr_b16 v[86:87], v0 offset:31232
	s_waitcnt lgkmcnt(14)
	v_add_f32_e32 v64, v70, v88
	v_add_f32_e32 v64, v71, v64
	v_add_f32_e32 v64, v72, v64
	v_add_f32_e32 v64, v73, v64
	v_cvt_pk_bf16_f32 v134, v68, v69
	v_cvt_pk_bf16_f32 v135, v70, v71
	ds_read_b64_tr_b16 v[88:89], v0 offset:27648
	ds_read_b64_tr_b16 v[90:91], v0 offset:28160
	s_waitcnt lgkmcnt(14)
	v_add_f32_e32 v64, v74, v64
	v_add_f32_e32 v64, v75, v64
	v_add_f32_e32 v64, v76, v64
	v_add_f32_e32 v64, v77, v64
	v_cvt_pk_bf16_f32 v128, v72, v73
	v_cvt_pk_bf16_f32 v129, v74, v75
	ds_read_b64_tr_b16 v[92:93], v0 offset:31744
	ds_read_b64_tr_b16 v[94:95], v0 offset:32256
	v_add_f32_e32 v0, v78, v64
	v_add_f32_e32 v0, v79, v0
	v_cvt_pk_bf16_f32 v130, v76, v77
	v_cvt_pk_bf16_f32 v131, v78, v79
	s_branch .Lna_D_2

.LBB0_660:
	s_cmp_lg_u32 s100, 0
	s_cbranch_scc1 .Lna_Bm_2
	s_cmp_lg_u32 s101, 0
	s_cbranch_scc1 .Lna_B1_2
	s_waitcnt lgkmcnt(14)
	v_mfma_f32_32x32x16_bf16 v[32:47], v[140:143], v[192:195], v[32:47]
	v_exp_f32_e32 v112, v112
	v_exp_f32_e32 v113, v113
	v_exp_f32_e32 v114, v114
	v_exp_f32_e32 v115, v115
	s_waitcnt lgkmcnt(12)
	v_mfma_f32_32x32x16_bf16 v[16:31], v[140:143], v[80:83], v[16:31]
	v_exp_f32_e32 v116, v116
	v_exp_f32_e32 v117, v117
	v_exp_f32_e32 v118, v118
	v_exp_f32_e32 v119, v119
	v_add_u32_e32 v64, s81, v227
	ds_read_b128 v[188:191], v64
	ds_read_b128 v[184:187], v64 offset:512
	s_waitcnt lgkmcnt(12)
	v_mfma_f32_32x32x16_bf16 v[32:47], v[136:139], v[2:5], v[32:47]
	v_exp_f32_e32 v120, v120
	v_exp_f32_e32 v121, v121
	v_exp_f32_e32 v122, v122
	v_exp_f32_e32 v123, v123
	ds_read_b128 v[180:183], v64 offset:2048
	ds_read_b128 v[176:179], v64 offset:2560
	s_waitcnt lgkmcnt(12)
	v_mfma_f32_32x32x16_bf16 v[16:31], v[136:139], v[6:9], v[16:31]
	v_exp_f32_e32 v124, v124
	v_exp_f32_e32 v125, v125
	v_exp_f32_e32 v126, v126
	v_exp_f32_e32 v127, v127
	ds_read_b128 v[172:175], v64 offset:4096
	ds_read_b128 v[168:171], v64 offset:4608
	s_waitcnt lgkmcnt(12)
	v_mfma_f32_32x32x16_bf16 v[32:47], v[132:135], v[10:13], v[32:47]
	v_exp_f32_e32 v96, v96
	v_exp_f32_e32 v97, v97
	v_exp_f32_e32 v98, v98
	v_exp_f32_e32 v99, v99
	ds_read_b128 v[164:167], v64 offset:6144
	ds_read_b128 v[160:163], v64 offset:6656
	s_waitcnt lgkmcnt(12)
	v_mfma_f32_32x32x16_bf16 v[16:31], v[132:135], v[84:87], v[16:31]
	v_exp_f32_e32 v100, v100
	v_exp_f32_e32 v101, v101
	v_exp_f32_e32 v102, v102
	v_exp_f32_e32 v103, v103
	s_waitcnt lgkmcnt(10)
	v_mfma_f32_32x32x16_bf16 v[32:47], v[128:131], v[88:91], v[32:47]
	v_exp_f32_e32 v104, v104
	v_exp_f32_e32 v105, v105
	v_exp_f32_e32 v106, v106
	v_exp_f32_e32 v107, v107
	s_waitcnt lgkmcnt(8)
	v_mfma_f32_32x32x16_bf16 v[16:31], v[128:131], v[92:95], v[16:31]
	v_exp_f32_e32 v108, v108
	v_exp_f32_e32 v109, v109
	v_exp_f32_e32 v110, v110
	v_exp_f32_e32 v111, v111
.Lna_Bend_2:
	s_mov_b64 s[46:47], -1
	s_and_b64 vcc, exec, s[44:45]
	s_cbranch_vccz .LBB0_725
	s_cmp_ge_i32 s50, s83
	s_cbranch_scc0 .LBB0_663
	s_waitcnt vmcnt(0) lgkmcnt(0)
	s_barrier
	s_mov_b64 s[46:47], 0

.LBB0_668:
	s_mov_b32 s101, s100
	s_mov_b32 s100, 0
	s_cmp_lt_u32 s50, 3
	s_cbranch_scc1 .Lna_ent_3
	s_add_i32 vcc_lo, s23, s90
	s_add_i32 vcc_lo, vcc_lo, -7
	s_cmp_gt_u32 vcc_lo, 7
	s_cselect_b32 s100, 1, 0
	s_cbranch_scc1 .Lna_skA_3

.Lna_D_3:
	s_cmp_ge_i32 s50, s26
	s_cselect_b64 s[46:47], -1, 0
	s_and_b64 vcc, exec, s[46:47]
	s_cbranch_vccnz .LBB0_670
	s_add_i32 s6, s81, s8
	s_mov_b32 s7, m0
	s_mov_b32 m0, s6
	s_nop 0
	global_load_lds_dwordx4 v[14:15], off
	s_mov_b32 m0, s7

.Lna_Bm_3:
	s_cmp_lg_u32 s101, 0
	s_cbranch_scc1 .Lna_B3_3
	s_waitcnt lgkmcnt(14)
	v_mfma_f32_32x32x16_bf16 v[32:47], v[140:143], v[200:203], v[32:47]
	s_waitcnt lgkmcnt(12)
	v_mfma_f32_32x32x16_bf16 v[16:31], v[140:143], v[196:199], v[16:31]
	v_cndmask_b32_e64 v0, 0, 1, s[48:49]
	v_cmp_ne_u32_e64 s[6:7], 1, v0
	s_andn2_b64 vcc, exec, s[48:49]
	v_add_u32_e32 v0, s64, v227
	s_cbranch_vccnz .Lna_b2_3_709
	ds_read_b128 v[188:191], v0
	ds_read_b128 v[184:187], v0 offset:512
.Lna_b2_3_709:
	s_waitcnt lgkmcnt(10)
	v_mfma_f32_32x32x16_bf16 v[32:47], v[136:139], v[192:195], v[32:47]
	s_and_b64 vcc, exec, s[6:7]
	s_cbranch_vccnz .Lna_b2_3_711
	ds_read_b128 v[180:183], v0 offset:2048
	ds_read_b128 v[176:179], v0 offset:2560
.Lna_b2_3_711:
	s_waitcnt lgkmcnt(8)
	v_mfma_f32_32x32x16_bf16 v[16:31], v[136:139], v[116:119], v[16:31]
	s_and_b64 vcc, exec, s[6:7]
	s_cbranch_vccnz .Lna_b2_3_713
	ds_read_b128 v[172:175], v0 offset:4096
	ds_read_b128 v[168:171], v0 offset:4608
.Lna_b2_3_713:
	s_waitcnt lgkmcnt(6)
	v_mfma_f32_32x32x16_bf16 v[32:47], v[132:135], v[112:115], v[32:47]
	s_and_b64 vcc, exec, s[6:7]
	s_cbranch_vccnz .Lna_b2_3_715
	ds_read_b128 v[164:167], v0 offset:6144
	ds_read_b128 v[160:163], v0 offset:6656
.Lna_b2_3_715:
	s_waitcnt lgkmcnt(4)
	v_mfma_f32_32x32x16_bf16 v[16:31], v[132:135], v[10:13], v[16:31]
	s_waitcnt lgkmcnt(2)
	v_mfma_f32_32x32x16_bf16 v[32:47], v[128:131], v[6:9], v[32:47]
	s_waitcnt lgkmcnt(0)
	v_mfma_f32_32x32x16_bf16 v[16:31], v[128:131], v[2:5], v[16:31]
	s_branch .Lna_Bend_3
.Lna_B3_3:
	s_waitcnt lgkmcnt(14)
	s_waitcnt lgkmcnt(12)
	v_cndmask_b32_e64 v0, 0, 1, s[48:49]
	v_cmp_ne_u32_e64 s[6:7], 1, v0
	s_andn2_b64 vcc, exec, s[48:49]
	v_add_u32_e32 v0, s64, v227
	s_cbranch_vccnz .Lna_b3_3_709
	ds_read_b128 v[188:191], v0
	ds_read_b128 v[184:187], v0 offset:512
.Lna_b3_3_709:
	s_waitcnt lgkmcnt(10)
	s_and_b64 vcc, exec, s[6:7]
	s_cbranch_vccnz .Lna_b3_3_711
	ds_read_b128 v[180:183], v0 offset:2048
	ds_read_b128 v[176:179], v0 offset:2560
.Lna_b3_3_711:
	s_waitcnt lgkmcnt(8)
	s_and_b64 vcc, exec, s[6:7]
	s_cbranch_vccnz .Lna_b3_3_713
	ds_read_b128 v[172:175], v0 offset:4096
	ds_read_b128 v[168:171], v0 offset:4608
.Lna_b3_3_713:
	s_waitcnt lgkmcnt(6)
	s_and_b64 vcc, exec, s[6:7]
	s_cbranch_vccnz .Lna_b3_3_715
	ds_read_b128 v[164:167], v0 offset:6144
	ds_read_b128 v[160:163], v0 offset:6656
.Lna_b3_3_715:
	s_waitcnt lgkmcnt(4)
	s_waitcnt lgkmcnt(2)
	s_waitcnt lgkmcnt(0)
	s_branch .Lna_Bend_3
.Lna_B1_3:
	s_waitcnt lgkmcnt(14)
	v_exp_f32_e32 v80, v80
	v_exp_f32_e32 v81, v81
	v_exp_f32_e32 v82, v82
	v_exp_f32_e32 v83, v83
	s_waitcnt lgkmcnt(12)
	v_exp_f32_e32 v84, v84
	v_exp_f32_e32 v85, v85
	v_exp_f32_e32 v86, v86
	v_exp_f32_e32 v87, v87
	v_cndmask_b32_e64 v0, 0, 1, s[48:49]
	v_cmp_ne_u32_e64 s[6:7], 1, v0
	s_andn2_b64 vcc, exec, s[48:49]
	v_add_u32_e32 v0, s64, v227
	s_cbranch_vccnz .Lna_b1_3_709
	ds_read_b128 v[188:191], v0
	ds_read_b128 v[184:187], v0 offset:512
.Lna_b1_3_709:
	s_waitcnt lgkmcnt(10)
	v_exp_f32_e32 v88, v88
	v_exp_f32_e32 v89, v89
	v_exp_f32_e32 v90, v90
	v_exp_f32_e32 v91, v91
	s_and_b64 vcc, exec, s[6:7]
	s_cbranch_vccnz .Lna_b1_3_711
	ds_read_b128 v[180:183], v0 offset:2048
	ds_read_b128 v[176:179], v0 offset:2560
.Lna_b1_3_711:
	s_waitcnt lgkmcnt(8)
	v_exp_f32_e32 v92, v92
	v_exp_f32_e32 v93, v93
	v_exp_f32_e32 v94, v94
	v_exp_f32_e32 v95, v95
	s_and_b64 vcc, exec, s[6:7]
	s_cbranch_vccnz .Lna_b1_3_713
	ds_read_b128 v[172:175], v0 offset:4096
	ds_read_b128 v[168:171], v0 offset:4608
.Lna_b1_3_713:
	s_waitcnt lgkmcnt(6)
	v_exp_f32_e32 v64, v64
	v_exp_f32_e32 v65, v65
	v_exp_f32_e32 v66, v66
	v_exp_f32_e32 v67, v67
	s_and_b64 vcc, exec, s[6:7]
	s_cbranch_vccnz .Lna_b1_3_715
	ds_read_b128 v[164:167], v0 offset:6144
	ds_read_b128 v[160:163], v0 offset:6656
.Lna_b1_3_715:
	s_waitcnt lgkmcnt(4)
	v_exp_f32_e32 v68, v68
	v_exp_f32_e32 v69, v69
	v_exp_f32_e32 v70, v70
	v_exp_f32_e32 v71, v71
	s_waitcnt lgkmcnt(2)
	v_exp_f32_e32 v72, v72
	v_exp_f32_e32 v73, v73
	v_exp_f32_e32 v74, v74
	v_exp_f32_e32 v75, v75
	s_waitcnt lgkmcnt(0)
	v_exp_f32_e32 v76, v76
	v_exp_f32_e32 v77, v77
	v_exp_f32_e32 v78, v78
	v_exp_f32_e32 v79, v79
	s_branch .Lna_Bend_3
.Lna_skA_3:
	v_add_u32_e32 v4, s64, v226
	ds_read_b64_tr_b16 v[200:201], v4 offset:24576
	ds_read_b64_tr_b16 v[202:203], v4 offset:25088
	s_waitcnt lgkmcnt(9)
	v_add_f32_e32 v2, v112, v113
	v_add_f32_e32 v2, v114, v2
	v_add_f32_e32 v2, v115, v2
	v_add_f32_e32 v2, v116, v2
	v_add_f32_e32 v2, v117, v2
	v_cvt_pk_bf16_f32 v140, v112, v113
	v_cvt_pk_bf16_f32 v141, v114, v115
	ds_read_b64_tr_b16 v[196:197], v4 offset:28672
	ds_read_b64_tr_b16 v[198:199], v4 offset:29184
	s_waitcnt lgkmcnt(10)
	v_add_f32_e32 v2, v118, v2
	v_add_f32_e32 v2, v119, v2
	v_add_f32_e32 v2, v120, v2
	v_add_f32_e32 v2, v121, v2
	v_cvt_pk_bf16_f32 v142, v116, v117
	v_cvt_pk_bf16_f32 v143, v118, v119
	ds_read_b64_tr_b16 v[192:193], v4 offset:25600
	ds_read_b64_tr_b16 v[194:195], v4 offset:26112
	s_waitcnt lgkmcnt(11)
	v_add_f32_e32 v2, v122, v2
	v_add_f32_e32 v2, v123, v2
	v_add_f32_e32 v2, v124, v2
	v_add_f32_e32 v2, v125, v2
	v_cvt_pk_bf16_f32 v136, v120, v121
	v_cvt_pk_bf16_f32 v137, v122, v123
	ds_read_b64_tr_b16 v[116:117], v4 offset:29696
	ds_read_b64_tr_b16 v[118:119], v4 offset:30208
	s_waitcnt lgkmcnt(12)
	v_add_f32_e32 v2, v126, v2
	v_add_f32_e32 v2, v127, v2
	v_add_f32_e32 v2, v96, v2
	v_add_f32_e32 v2, v97, v2
	v_cvt_pk_bf16_f32 v138, v124, v125
	v_cvt_pk_bf16_f32 v139, v126, v127
	ds_read_b64_tr_b16 v[112:113], v4 offset:26624
	ds_read_b64_tr_b16 v[114:115], v4 offset:27136
	s_waitcnt lgkmcnt(13)
	v_add_f32_e32 v2, v98, v2
	v_add_f32_e32 v2, v99, v2
	v_add_f32_e32 v2, v100, v2
	v_add_f32_e32 v2, v101, v2
	v_cvt_pk_bf16_f32 v132, v96, v97
	v_cvt_pk_bf16_f32 v133, v98, v99
	ds_read_b64_tr_b16 v[10:11], v4 offset:30720
	ds_read_b64_tr_b16 v[12:13], v4 offset:31232
	s_waitcnt lgkmcnt(14)
	v_add_f32_e32 v2, v102, v2
	v_add_f32_e32 v2, v103, v2
	v_add_f32_e32 v2, v104, v2
	v_add_f32_e32 v2, v105, v2
	v_cvt_pk_bf16_f32 v134, v100, v101
	v_cvt_pk_bf16_f32 v135, v102, v103
	ds_read_b64_tr_b16 v[6:7], v4 offset:27648
	ds_read_b64_tr_b16 v[8:9], v4 offset:28160
	s_waitcnt lgkmcnt(14)
	v_add_f32_e32 v2, v106, v2
	v_add_f32_e32 v2, v107, v2
	v_add_f32_e32 v2, v108, v2
	v_add_f32_e32 v96, v109, v2
	v_cvt_pk_bf16_f32 v128, v104, v105
	v_cvt_pk_bf16_f32 v129, v106, v107
	ds_read_b64_tr_b16 v[2:3], v4 offset:31744
	ds_read_b64_tr_b16 v[4:5], v4 offset:32256
	v_add_f32_e32 v96, v110, v96
	v_add_f32_e32 v96, v111, v96
	v_add_f32_e32 v120, 0, v96
	v_cvt_pk_bf16_f32 v130, v108, v109
	v_cvt_pk_bf16_f32 v131, v110, v111
	s_branch .Lna_D_3

.LBB0_707:
	s_cmp_lg_u32 s100, 0
	s_cbranch_scc1 .Lna_Bm_3
	s_cmp_lg_u32 s101, 0
	s_cbranch_scc1 .Lna_B1_3
	s_waitcnt lgkmcnt(14)
	v_mfma_f32_32x32x16_bf16 v[32:47], v[140:143], v[200:203], v[32:47]
	v_exp_f32_e32 v80, v80
	v_exp_f32_e32 v81, v81
	v_exp_f32_e32 v82, v82
	v_exp_f32_e32 v83, v83
	s_waitcnt lgkmcnt(12)
	v_mfma_f32_32x32x16_bf16 v[16:31], v[140:143], v[196:199], v[16:31]
	v_exp_f32_e32 v84, v84
	v_exp_f32_e32 v85, v85
	v_exp_f32_e32 v86, v86
	v_exp_f32_e32 v87, v87
	v_cndmask_b32_e64 v0, 0, 1, s[48:49]
	v_cmp_ne_u32_e64 s[6:7], 1, v0
	s_andn2_b64 vcc, exec, s[48:49]
	v_add_u32_e32 v0, s64, v227
	s_cbranch_vccnz .LBB0_709
	ds_read_b128 v[188:191], v0
	ds_read_b128 v[184:187], v0 offset:512

.Lna_Bend_3:
	s_mov_b64 s[6:7], -1
	s_and_b64 vcc, exec, s[46:47]
	s_cbranch_vccz .LBB0_727
	s_and_b64 vcc, exec, s[44:45]
	s_cbranch_vccz .LBB0_718
	s_waitcnt vmcnt(0) lgkmcnt(0)
	s_barrier
	s_mov_b64 s[6:7], 0

.LBB0_737:
	s_mov_b32 s101, s100
	s_mov_b32 s100, 0
	s_cmp_lt_i32 s0, 5
	s_cbranch_scc1 .Lna_ent_4
	s_add_i32 vcc_lo, s65, s63
	s_max_i32 vcc_lo, vcc_lo, 4
	s_add_i32 vcc_lo, vcc_lo, -4
	s_min_u32 vcc_lo, vcc_lo, 56
	s_add_i32 vcc_hi, s13, s12
	s_sub_i32 vcc_lo, vcc_hi, vcc_lo
	s_cmp_gt_u32 vcc_lo, 7
	s_cselect_b32 s100, 1, 0
	s_cbranch_scc1 .Lna_skA_4

.Lna_D_4:
	s_cmp_lt_i32 s0, 5
	s_cbranch_scc1 .LBB0_771
	s_add_i32 s65, s65, s63
	s_max_i32 s0, s65, 4
	s_add_i32 s0, s0, -4
	s_min_u32 s0, s0, 56
	s_add_i32 s13, s13, s12
	s_sub_i32 s0, s13, s0
	s_cmp_gt_u32 s0, 7
	s_cselect_b64 vcc, -1, 0
	s_cbranch_scc1 .Lna_allmask_4
	s_sub_i32 s0, s13, s65
	s_max_i32 s0, s0, -7
	s_add_i32 s0, s0, 7
	s_min_u32 s0, s0, 14
	s_mulk_i32 s0, 0x7c
	v_lshlrev_b32_e32 v14, 2, v224
	v_add3_u32 v116, v225, s0, v14
	v_lshlrev_b32_e32 v76, 2, v223
	v_add_u32_e32 v76, 0x16100, v76
	ds_read_b32 v64, v116
	ds_read_b32 v70, v76
	ds_read_b32 v65, v116 offset:4
	ds_read_b32 v71, v76 offset:4
	ds_read_b32 v66, v116 offset:8
	ds_read_b32 v72, v76 offset:8
	ds_read_b32 v67, v116 offset:12
	ds_read_b32 v73, v76 offset:12
	ds_read_b32 v68, v116 offset:32
	ds_read_b32 v74, v76 offset:32
	ds_read_b32 v69, v116 offset:36
	ds_read_b32 v75, v76 offset:36
	s_waitcnt lgkmcnt(10)
	v_add_f32_e32 v96, v96, v64
	v_add_f32_e32 v96, v96, v70
	ds_read_b32 v64, v116 offset:40
	ds_read_b32 v70, v76 offset:40
	s_waitcnt lgkmcnt(10)
	v_add_f32_e32 v97, v97, v65
	v_add_f32_e32 v97, v97, v71
	ds_read_b32 v65, v116 offset:44
	ds_read_b32 v71, v76 offset:44
	s_waitcnt lgkmcnt(10)
	v_add_f32_e32 v98, v98, v66
	v_add_f32_e32 v98, v98, v72
	ds_read_b32 v66, v116 offset:64
	ds_read_b32 v72, v76 offset:64
	s_waitcnt lgkmcnt(10)
	v_add_f32_e32 v99, v99, v67
	v_add_f32_e32 v99, v99, v73
	ds_read_b32 v67, v116 offset:68
	ds_read_b32 v73, v76 offset:68
	s_waitcnt lgkmcnt(10)
	v_add_f32_e32 v100, v100, v68
	v_add_f32_e32 v100, v100, v74
	ds_read_b32 v68, v116 offset:72
	ds_read_b32 v74, v76 offset:72
	s_waitcnt lgkmcnt(10)
	v_add_f32_e32 v101, v101, v69
	v_add_f32_e32 v101, v101, v75
	ds_read_b32 v69, v116 offset:76
	ds_read_b32 v75, v76 offset:76
	s_waitcnt lgkmcnt(10)
	v_add_f32_e32 v102, v102, v64
	v_add_f32_e32 v102, v102, v70
	ds_read_b32 v64, v116 offset:96
	ds_read_b32 v70, v76 offset:96
	s_waitcnt lgkmcnt(10)
	v_add_f32_e32 v103, v103, v65
	v_add_f32_e32 v103, v103, v71
	ds_read_b32 v65, v116 offset:100
	ds_read_b32 v71, v76 offset:100
	s_waitcnt lgkmcnt(10)
	v_add_f32_e32 v104, v104, v66
	v_add_f32_e32 v104, v104, v72
	ds_read_b32 v66, v116 offset:104
	ds_read_b32 v72, v76 offset:104
	s_waitcnt lgkmcnt(10)
	v_add_f32_e32 v105, v105, v67
	v_add_f32_e32 v105, v105, v73
	ds_read_b32 v67, v116 offset:108
	ds_read_b32 v73, v76 offset:108
	s_waitcnt lgkmcnt(10)
	v_add_f32_e32 v106, v106, v68
	v_add_f32_e32 v106, v106, v74
	ds_read_b32 v68, v116 offset:128
	ds_read_b32 v74, v76 offset:128
	s_waitcnt lgkmcnt(10)
	v_add_f32_e32 v107, v107, v69
	v_add_f32_e32 v107, v107, v75
	ds_read_b32 v69, v116 offset:132
	ds_read_b32 v75, v76 offset:132
	s_waitcnt lgkmcnt(10)
	v_add_f32_e32 v108, v108, v64
	v_add_f32_e32 v108, v108, v70
	ds_read_b32 v64, v116 offset:136
	ds_read_b32 v70, v76 offset:136
	s_waitcnt lgkmcnt(10)
	v_add_f32_e32 v109, v109, v65
	v_add_f32_e32 v109, v109, v71
	ds_read_b32 v65, v116 offset:140
	ds_read_b32 v71, v76 offset:140
	s_waitcnt lgkmcnt(10)
	v_add_f32_e32 v110, v110, v66
	v_add_f32_e32 v110, v110, v72
	ds_read_b32 v66, v116 offset:160
	ds_read_b32 v72, v76 offset:160
	s_waitcnt lgkmcnt(10)
	v_add_f32_e32 v111, v111, v67
	v_add_f32_e32 v111, v111, v73
	ds_read_b32 v67, v116 offset:164
	ds_read_b32 v73, v76 offset:164
	s_waitcnt lgkmcnt(10)
	v_add_f32_e32 v48, v48, v68
	v_add_f32_e32 v48, v48, v74
	ds_read_b32 v68, v116 offset:168
	ds_read_b32 v74, v76 offset:168
	s_waitcnt lgkmcnt(10)
	v_add_f32_e32 v49, v49, v69
	v_add_f32_e32 v49, v49, v75
	ds_read_b32 v69, v116 offset:172
	ds_read_b32 v75, v76 offset:172
	s_waitcnt lgkmcnt(10)
	v_add_f32_e32 v50, v50, v64
	v_add_f32_e32 v50, v50, v70
	ds_read_b32 v64, v116 offset:192
	ds_read_b32 v70, v76 offset:192
	s_waitcnt lgkmcnt(10)
	v_add_f32_e32 v51, v51, v65
	v_add_f32_e32 v51, v51, v71
	ds_read_b32 v65, v116 offset:196
	ds_read_b32 v71, v76 offset:196
	s_waitcnt lgkmcnt(10)
	v_add_f32_e32 v52, v52, v66
	v_add_f32_e32 v52, v52, v72
	ds_read_b32 v66, v116 offset:200
	ds_read_b32 v72, v76 offset:200
	s_waitcnt lgkmcnt(10)
	v_add_f32_e32 v53, v53, v67
	v_add_f32_e32 v53, v53, v73
	ds_read_b32 v67, v116 offset:204
	ds_read_b32 v73, v76 offset:204
	s_waitcnt lgkmcnt(10)
	v_add_f32_e32 v54, v54, v68
	v_add_f32_e32 v54, v54, v74
	ds_read_b32 v68, v116 offset:224
	ds_read_b32 v74, v76 offset:224
	s_waitcnt lgkmcnt(10)
	v_add_f32_e32 v55, v55, v69
	v_add_f32_e32 v55, v55, v75
	ds_read_b32 v69, v116 offset:228
	ds_read_b32 v75, v76 offset:228
	s_waitcnt lgkmcnt(10)
	v_add_f32_e32 v56, v56, v64
	v_add_f32_e32 v56, v56, v70
	ds_read_b32 v64, v116 offset:232
	ds_read_b32 v70, v76 offset:232
	s_waitcnt lgkmcnt(10)
	v_add_f32_e32 v57, v57, v65
	v_add_f32_e32 v57, v57, v71
	ds_read_b32 v65, v116 offset:236
	ds_read_b32 v71, v76 offset:236
	s_waitcnt lgkmcnt(10)
	v_add_f32_e32 v58, v58, v66
	v_add_f32_e32 v58, v58, v72
	s_waitcnt lgkmcnt(8)
	v_add_f32_e32 v59, v59, v67
	v_add_f32_e32 v59, v59, v73
	s_waitcnt lgkmcnt(6)
	v_add_f32_e32 v60, v60, v68
	v_add_f32_e32 v60, v60, v74
	s_waitcnt lgkmcnt(4)
	v_add_f32_e32 v61, v61, v69
	v_add_f32_e32 v61, v61, v75
	s_waitcnt lgkmcnt(2)
	v_add_f32_e32 v62, v62, v64
	v_add_f32_e32 v62, v62, v70
	s_waitcnt lgkmcnt(0)
	v_add_f32_e32 v63, v63, v65
	v_add_f32_e32 v63, v63, v71
	s_branch .LBB0_771
.Lna_Bm_4:
	s_cmp_lg_u32 s101, 0
	s_cbranch_scc1 .Lna_B3_4
	s_waitcnt lgkmcnt(14)
	v_mfma_f32_32x32x16_bf16 v[32:47], v[140:143], v[6:9], v[32:47]
	s_waitcnt lgkmcnt(12)
	v_mfma_f32_32x32x16_bf16 v[16:31], v[140:143], v[2:5], v[16:31]
	s_waitcnt lgkmcnt(10)
	v_mfma_f32_32x32x16_bf16 v[32:47], v[136:139], v[10:13], v[32:47]
	s_waitcnt lgkmcnt(8)
	v_mfma_f32_32x32x16_bf16 v[16:31], v[136:139], v[80:83], v[16:31]
	s_waitcnt lgkmcnt(6)
	v_mfma_f32_32x32x16_bf16 v[32:47], v[132:135], v[84:87], v[32:47]
	s_waitcnt lgkmcnt(4)
	v_mfma_f32_32x32x16_bf16 v[16:31], v[132:135], v[88:91], v[16:31]
	s_waitcnt lgkmcnt(2)
	v_mfma_f32_32x32x16_bf16 v[32:47], v[128:131], v[92:95], v[32:47]
	s_waitcnt lgkmcnt(0)
	v_mfma_f32_32x32x16_bf16 v[16:31], v[128:131], v[112:115], v[16:31]
	s_branch .Lna_Bend_4
.Lna_B3_4:
	s_waitcnt lgkmcnt(14)
	s_waitcnt lgkmcnt(12)
	s_waitcnt lgkmcnt(10)
	s_waitcnt lgkmcnt(8)
	s_waitcnt lgkmcnt(6)
	s_waitcnt lgkmcnt(4)
	s_waitcnt lgkmcnt(2)
	s_waitcnt lgkmcnt(0)
	s_branch .Lna_Bend_4
.Lna_B1_4:
	s_waitcnt lgkmcnt(14)
	v_exp_f32_e32 v96, v96
	v_exp_f32_e32 v97, v97
	v_exp_f32_e32 v98, v98
	v_exp_f32_e32 v99, v99
	s_waitcnt lgkmcnt(12)
	v_exp_f32_e32 v100, v100
	v_exp_f32_e32 v101, v101
	v_exp_f32_e32 v102, v102
	v_exp_f32_e32 v103, v103
	s_waitcnt lgkmcnt(10)
	v_exp_f32_e32 v104, v104
	v_exp_f32_e32 v105, v105
	v_exp_f32_e32 v106, v106
	v_exp_f32_e32 v107, v107
	s_waitcnt lgkmcnt(8)
	v_exp_f32_e32 v108, v108
	v_exp_f32_e32 v109, v109
	v_exp_f32_e32 v110, v110
	v_exp_f32_e32 v111, v111
	s_waitcnt lgkmcnt(6)
	v_exp_f32_e32 v48, v48
	v_exp_f32_e32 v49, v49
	v_exp_f32_e32 v50, v50
	v_exp_f32_e32 v51, v51
	s_waitcnt lgkmcnt(4)
	v_exp_f32_e32 v52, v52
	v_exp_f32_e32 v53, v53
	v_exp_f32_e32 v54, v54
	v_exp_f32_e32 v55, v55
	s_waitcnt lgkmcnt(2)
	v_exp_f32_e32 v56, v56
	v_exp_f32_e32 v57, v57
	v_exp_f32_e32 v58, v58
	v_exp_f32_e32 v59, v59
	s_waitcnt lgkmcnt(0)
	v_exp_f32_e32 v60, v60
	v_exp_f32_e32 v61, v61
	v_exp_f32_e32 v62, v62
	v_exp_f32_e32 v63, v63
	s_branch .Lna_Bend_4
.Lna_skA_4:
	v_add_u32_e32 v0, s81, v226
	ds_read_b64_tr_b16 v[6:7], v0 offset:24576
	ds_read_b64_tr_b16 v[8:9], v0 offset:25088
	s_waitcnt lgkmcnt(9)
	v_add_f32_e32 v2, v80, v81
	v_add_f32_e32 v2, v82, v2
	v_add_f32_e32 v2, v83, v2
	v_add_f32_e32 v2, v84, v2
	v_add_f32_e32 v10, v85, v2
	v_cvt_pk_bf16_f32 v140, v80, v81
	v_cvt_pk_bf16_f32 v141, v82, v83
	ds_read_b64_tr_b16 v[2:3], v0 offset:28672
	ds_read_b64_tr_b16 v[4:5], v0 offset:29184
	s_waitcnt lgkmcnt(10)
	v_add_f32_e32 v10, v86, v10
	v_add_f32_e32 v10, v87, v10
	v_add_f32_e32 v10, v88, v10
	v_add_f32_e32 v14, v89, v10
	v_cvt_pk_bf16_f32 v142, v84, v85
	v_cvt_pk_bf16_f32 v143, v86, v87
	ds_read_b64_tr_b16 v[10:11], v0 offset:25600
	ds_read_b64_tr_b16 v[12:13], v0 offset:26112
	s_waitcnt lgkmcnt(11)
	v_add_f32_e32 v14, v90, v14
	v_add_f32_e32 v14, v91, v14
	v_add_f32_e32 v14, v92, v14
	v_add_f32_e32 v14, v93, v14
	v_cvt_pk_bf16_f32 v136, v88, v89
	v_cvt_pk_bf16_f32 v137, v90, v91
	ds_read_b64_tr_b16 v[80:81], v0 offset:29696
	ds_read_b64_tr_b16 v[82:83], v0 offset:30208
	s_waitcnt lgkmcnt(12)
	v_add_f32_e32 v14, v94, v14
	v_add_f32_e32 v14, v95, v14
	v_add_f32_e32 v14, v64, v14
	v_add_f32_e32 v14, v65, v14
	v_cvt_pk_bf16_f32 v138, v92, v93
	v_cvt_pk_bf16_f32 v139, v94, v95
	ds_read_b64_tr_b16 v[84:85], v0 offset:26624
	ds_read_b64_tr_b16 v[86:87], v0 offset:27136
	s_waitcnt lgkmcnt(13)
	v_add_f32_e32 v14, v66, v14
	v_add_f32_e32 v14, v67, v14
	v_add_f32_e32 v14, v68, v14
	v_add_f32_e32 v14, v69, v14
	v_cvt_pk_bf16_f32 v132, v64, v65
	v_cvt_pk_bf16_f32 v133, v66, v67
	ds_read_b64_tr_b16 v[88:89], v0 offset:30720
	ds_read_b64_tr_b16 v[90:91], v0 offset:31232
	s_waitcnt lgkmcnt(14)
	v_add_f32_e32 v14, v70, v14
	v_add_f32_e32 v14, v71, v14
	v_add_f32_e32 v14, v72, v14
	v_add_f32_e32 v14, v73, v14
	v_cvt_pk_bf16_f32 v134, v68, v69
	v_cvt_pk_bf16_f32 v135, v70, v71
	ds_read_b64_tr_b16 v[92:93], v0 offset:27648
	ds_read_b64_tr_b16 v[94:95], v0 offset:28160
	s_waitcnt lgkmcnt(14)
	v_add_f32_e32 v14, v74, v14
	v_add_f32_e32 v14, v75, v14
	v_add_f32_e32 v14, v76, v14
	v_add_f32_e32 v14, v77, v14
	v_cvt_pk_bf16_f32 v128, v72, v73
	v_cvt_pk_bf16_f32 v129, v74, v75
	ds_read_b64_tr_b16 v[112:113], v0 offset:31744
	ds_read_b64_tr_b16 v[114:115], v0 offset:32256
	v_add_f32_e32 v0, v78, v14
	v_add_f32_e32 v0, v79, v0
	v_cvt_pk_bf16_f32 v130, v76, v77
	v_cvt_pk_bf16_f32 v131, v78, v79
	s_branch .Lna_D_4
.Lna_allmask_4:
	v_mov_b32_e32 v96, 0
	v_mov_b32_e32 v97, 0
	v_mov_b32_e32 v98, 0
	v_mov_b32_e32 v99, 0
	v_mov_b32_e32 v100, 0
	v_mov_b32_e32 v101, 0
	v_mov_b32_e32 v102, 0
	v_mov_b32_e32 v103, 0
	v_mov_b32_e32 v104, 0
	v_mov_b32_e32 v105, 0
	v_mov_b32_e32 v106, 0
	v_mov_b32_e32 v107, 0
	v_mov_b32_e32 v108, 0
	v_mov_b32_e32 v109, 0
	v_mov_b32_e32 v110, 0
	v_mov_b32_e32 v111, 0
	v_mov_b32_e32 v48, 0
	v_mov_b32_e32 v49, 0
	v_mov_b32_e32 v50, 0
	v_mov_b32_e32 v51, 0
	v_mov_b32_e32 v52, 0
	v_mov_b32_e32 v53, 0
	v_mov_b32_e32 v54, 0
	v_mov_b32_e32 v55, 0
	v_mov_b32_e32 v56, 0
	v_mov_b32_e32 v57, 0
	v_mov_b32_e32 v58, 0
	v_mov_b32_e32 v59, 0
	v_mov_b32_e32 v60, 0
	v_mov_b32_e32 v61, 0
	v_mov_b32_e32 v62, 0
	v_mov_b32_e32 v63, 0

.LBB0_772:
	s_cmp_lg_u32 s100, 0
	s_cbranch_scc1 .Lna_Bm_4
	s_cmp_lg_u32 s101, 0
	s_cbranch_scc1 .Lna_B1_4
	s_waitcnt lgkmcnt(14)
	v_mfma_f32_32x32x16_bf16 v[32:47], v[140:143], v[6:9], v[32:47]
	v_exp_f32_e32 v96, v96
	v_exp_f32_e32 v97, v97
	v_exp_f32_e32 v98, v98
	v_exp_f32_e32 v99, v99
	s_waitcnt lgkmcnt(12)
	v_mfma_f32_32x32x16_bf16 v[16:31], v[140:143], v[2:5], v[16:31]
	v_exp_f32_e32 v100, v100
	v_exp_f32_e32 v101, v101
	v_exp_f32_e32 v102, v102
	v_exp_f32_e32 v103, v103
	s_waitcnt lgkmcnt(10)
	v_mfma_f32_32x32x16_bf16 v[32:47], v[136:139], v[10:13], v[32:47]
	v_exp_f32_e32 v104, v104
	v_exp_f32_e32 v105, v105
	v_exp_f32_e32 v106, v106
	v_exp_f32_e32 v107, v107
	s_waitcnt lgkmcnt(8)
	v_mfma_f32_32x32x16_bf16 v[16:31], v[136:139], v[80:83], v[16:31]
	v_exp_f32_e32 v108, v108
	v_exp_f32_e32 v109, v109
	v_exp_f32_e32 v110, v110
	v_exp_f32_e32 v111, v111
	s_waitcnt lgkmcnt(6)
	v_mfma_f32_32x32x16_bf16 v[32:47], v[132:135], v[84:87], v[32:47]
	v_exp_f32_e32 v48, v48
	v_exp_f32_e32 v49, v49
	v_exp_f32_e32 v50, v50
	v_exp_f32_e32 v51, v51
	s_waitcnt lgkmcnt(4)
	v_mfma_f32_32x32x16_bf16 v[16:31], v[132:135], v[88:91], v[16:31]
	v_exp_f32_e32 v52, v52
	v_exp_f32_e32 v53, v53
	v_exp_f32_e32 v54, v54
	v_exp_f32_e32 v55, v55
	s_waitcnt lgkmcnt(2)
	v_mfma_f32_32x32x16_bf16 v[32:47], v[128:131], v[92:95], v[32:47]
	v_exp_f32_e32 v56, v56
	v_exp_f32_e32 v57, v57
	v_exp_f32_e32 v58, v58
	v_exp_f32_e32 v59, v59
	s_waitcnt lgkmcnt(0)
	v_mfma_f32_32x32x16_bf16 v[16:31], v[128:131], v[112:115], v[16:31]
	v_exp_f32_e32 v60, v60
	v_exp_f32_e32 v61, v61
	v_exp_f32_e32 v62, v62
	v_exp_f32_e32 v63, v63
.Lna_Bend_4:
	s_andn2_b64 vcc, exec, s[4:5]
	s_cbranch_vccnz .LBB0_774
	s_waitcnt lgkmcnt(0)
	ds_read_b128 v[2:5], v220 offset:49248
	ds_read_b128 v[6:9], v220 offset:49216
	ds_read_b128 v[10:13], v220 offset:49184
	ds_read_b128 v[64:67], v220 offset:49152
	s_waitcnt lgkmcnt(3)
	v_pk_mul_f32 v[46:47], v[46:47], v[4:5]
	s_waitcnt lgkmcnt(2)
	v_pk_mul_f32 v[42:43], v[42:43], v[8:9]
	s_waitcnt lgkmcnt(1)
	v_pk_mul_f32 v[38:39], v[38:39], v[12:13]
	s_waitcnt lgkmcnt(0)
	v_pk_mul_f32 v[34:35], v[34:35], v[66:67]
	v_pk_mul_f32 v[44:45], v[44:45], v[2:3]
	v_pk_mul_f32 v[40:41], v[40:41], v[6:7]
	v_pk_mul_f32 v[36:37], v[36:37], v[10:11]
	v_pk_mul_f32 v[32:33], v[32:33], v[64:65]
	v_pk_mul_f32 v[30:31], v[30:31], v[4:5]
	v_pk_mul_f32 v[26:27], v[26:27], v[8:9]
	v_pk_mul_f32 v[22:23], v[22:23], v[12:13]
	v_pk_mul_f32 v[18:19], v[18:19], v[66:67]
	v_pk_mul_f32 v[28:29], v[28:29], v[2:3]
	v_pk_mul_f32 v[24:25], v[24:25], v[6:7]
	v_pk_mul_f32 v[20:21], v[20:21], v[10:11]
	v_pk_mul_f32 v[16:17], v[16:17], v[64:65]

	.amdhsa_kernel _Z6mk_fwd6MkArgs
		.amdhsa_group_segment_fixed_size 0
		.amdhsa_private_segment_fixed_size 0
		.amdhsa_kernarg_size 472
		.amdhsa_user_sgpr_count 2
		.amdhsa_user_sgpr_dispatch_ptr 0
		.amdhsa_user_sgpr_queue_ptr 0
		.amdhsa_user_sgpr_kernarg_segment_ptr 1
		.amdhsa_user_sgpr_dispatch_id 0
		.amdhsa_user_sgpr_kernarg_preload_length 0
		.amdhsa_user_sgpr_kernarg_preload_offset 0
		.amdhsa_user_sgpr_private_segment_size 0
		.amdhsa_uses_dynamic_stack 0
		.amdhsa_enable_private_segment 0
		.amdhsa_system_sgpr_workgroup_id_x 1
		.amdhsa_system_sgpr_workgroup_id_y 0
		.amdhsa_system_sgpr_workgroup_id_z 0
		.amdhsa_system_sgpr_workgroup_info 0
		.amdhsa_system_vgpr_workitem_id 0
		.amdhsa_next_free_vgpr 256
		.amdhsa_next_free_sgpr 102
		.amdhsa_accum_offset 256
		.amdhsa_reserve_vcc 1
		.amdhsa_float_round_mode_32 0
		.amdhsa_float_round_mode_16_64 0
		.amdhsa_float_denorm_mode_32 3
		.amdhsa_float_denorm_mode_16_64 3
		.amdhsa_dx10_clamp 1
		.amdhsa_ieee_mode 1
		.amdhsa_fp16_overflow 0
		.amdhsa_tg_split 0
		.amdhsa_exception_fp_ieee_invalid_op 0
		.amdhsa_exception_fp_denorm_src 0
		.amdhsa_exception_fp_ieee_div_zero 0
		.amdhsa_exception_fp_ieee_overflow 0
		.amdhsa_exception_fp_ieee_underflow 0
		.amdhsa_exception_fp_ieee_inexact 0
		.amdhsa_exception_int_div_zero 0
	.end_amdhsa_kernel

amdhsa.kernels:
  - .agpr_count:     0
    .args:
      - .offset:         0
        .size:           216
        .value_kind:     by_value
      - .offset:         216
        .size:           4
        .value_kind:     hidden_block_count_x
      - .offset:         220
        .size:           4
        .value_kind:     hidden_block_count_y
      - .offset:         224
        .size:           4
        .value_kind:     hidden_block_count_z
      - .offset:         228
        .size:           2
        .value_kind:     hidden_group_size_x
      - .offset:         230
        .size:           2
        .value_kind:     hidden_group_size_y
      - .offset:         232
        .size:           2
        .value_kind:     hidden_group_size_z
      - .offset:         234
        .size:           2
        .value_kind:     hidden_remainder_x
      - .offset:         236
        .size:           2
        .value_kind:     hidden_remainder_y
      - .offset:         238
        .size:           2
        .value_kind:     hidden_remainder_z
      - .offset:         256
        .size:           8
        .value_kind:     hidden_global_offset_x
      - .offset:         264
        .size:           8
        .value_kind:     hidden_global_offset_y
      - .offset:         272
        .size:           8
        .value_kind:     hidden_global_offset_z
      - .offset:         280
        .size:           2
        .value_kind:     hidden_grid_dims
      - .offset:         336
        .size:           4
        .value_kind:     hidden_dynamic_lds_size
    .group_segment_fixed_size: 0
    .kernarg_segment_align: 8
    .kernarg_segment_size: 472
    .language:       OpenCL C
    .language_version:
      - 2
      - 0
    .max_flat_workgroup_size: 512
    .name:           _Z6mk_fwd6MkArgs
    .private_segment_fixed_size: 0
    .sgpr_count:     108
    .sgpr_spill_count: 261
    .symbol:         _Z6mk_fwd6MkArgs.kd
    .uniform_work_group_size: 1
    .uses_dynamic_stack: false
    .vgpr_count:     256
    .vgpr_spill_count: 0
    .wavefront_size: 64
